# P13: S5 waves convert 2 rows per wave of the layer-1 u table after their chains (conversion-wave loop shortened accordingly)
# baseline (speedup 1.0000x reference)
; __device__ __forceinline__ void peer_row_load(f32x4 (&v)[16], const float* const (&in)[34], int it, int layer, int lane) {
;     const int tbl = it >= NEXP, r = it - tbl * NEXP + layer * NEXP;
;     const f32x4* src = (const f32x4*)((tbl ? in[33] : in[32]) + (size_t)r * D) + lane;
; #pragma unroll
;     for (int j = 0; j < 16; ++j) v[j] = src[64 * j];
;     f32x4 va[16], vb[16];
;     if (it_lo + gw >= it_hi) return;
;     peer_row_load(va, in, it_lo + gw, only_layer, lane);
; #pragma unroll 1
;     for (int it = it_lo + gw; it < it_hi; it += 2 * NGW) {
;         const int it1 = it + NGW, it2 = it + 2 * NGW;
;         peer_row_load(vb, in, it1 < it_hi ? it1 : it, only_layer, lane);
.LBB0_1486:
	v_mov_b32_e32 v1, v0
	s_nop 0
	v_readfirstlane_b32 s0, v1
	s_ashr_i32 s0, s0, 6
	s_cmp_lt_i32 s0, 4
	s_cbranch_scc1 .Lp13_conv
	s_lshl_b32 s1, s2, 2
	s_add_i32 s0, s1, s0
	s_add_i32 s4, s0, -4
	s_lshl_b32 s3, s34, 2
	s_cmpk_gt_i32 s4, 0x37ff
	v_and_b32_e32 v130, 63, v1
	s_cbranch_scc1 .LBB0_1496
	s_ashr_i32 s5, s4, 31
	s_lshl_b64 s[0:1], s[4:5], 14
	s_add_u32 s0, s84, s0
	s_addc_u32 s1, s85, s1
	v_mov_b32_e32 v133, 0
	v_lshlrev_b32_e32 v132, 4, v130
	v_lshl_add_u64 v[2:3], s[0:1], 0, v[132:133]
	s_mov_b64 s[0:1], 0x10000000
	v_add_co_u32_e32 v6, vcc, 0x10000000, v2
	v_lshl_add_u64 v[4:5], v[2:3], 0, s[0:1]
	s_nop 0
	v_addc_co_u32_e32 v7, vcc, 0, v3, vcc
	global_load_dwordx4 v[62:65], v[4:5], off offset:1024
	global_load_dwordx4 v[46:49], v[4:5], off offset:2048
	global_load_dwordx4 v[86:89], v[6:7], off
	global_load_dwordx4 v[54:57], v[4:5], off offset:3072
	v_add_co_u32_e32 v4, vcc, 0x10001000, v2
	v_lshlrev_b32_e32 v132, 2, v130
	s_nop 0
	v_addc_co_u32_e32 v5, vcc, 0, v3, vcc
	global_load_dwordx4 v[50:53], v[4:5], off
	global_load_dwordx4 v[42:45], v[4:5], off offset:1024
	global_load_dwordx4 v[34:37], v[4:5], off offset:2048
	global_load_dwordx4 v[38:41], v[4:5], off offset:3072
	v_add_co_u32_e32 v4, vcc, 0x10002000, v2
	s_mov_b64 s[0:1], 0xba00000
	s_nop 0
	v_addc_co_u32_e32 v5, vcc, 0, v3, vcc
	v_add_co_u32_e32 v58, vcc, 0x10003000, v2
	global_load_dwordx4 v[30:33], v[4:5], off
	global_load_dwordx4 v[26:29], v[4:5], off offset:1024
	global_load_dwordx4 v[22:25], v[4:5], off offset:2048
	global_load_dwordx4 v[14:17], v[4:5], off offset:3072
	v_addc_co_u32_e32 v59, vcc, 0, v3, vcc
	global_load_dwordx4 v[18:21], v[58:59], off
	global_load_dwordx4 v[10:13], v[58:59], off offset:1024
	global_load_dwordx4 v[6:9], v[58:59], off offset:2048
	global_load_dwordx4 v[2:5], v[58:59], off offset:3072
	v_lshl_add_u64 v[58:59], s[90:91], 0, v[132:133]
	s_add_u32 s5, s90, 0x1ba00000
	v_lshl_add_u64 v[134:135], v[58:59], 0, s[0:1]
	v_cmp_eq_u32_e64 s[0:1], 0, v130
	s_addc_u32 s12, s91, 0
	s_lshl_b32 s13, s34, 3
	s_movk_i32 s14, 0x1000
	s_movk_i32 s15, 0x2000
	s_movk_i32 s16, 0x3000
	s_mov_b32 s17, 0x43800000
	s_mov_b32 s19, s4
	s_branch .LBB0_1491

; __device__ __forceinline__ void peer_row_load(f32x4 (&v)[16], const float* const (&in)[34], int it, int layer, int lane) {
;     const int tbl = it >= NEXP, r = it - tbl * NEXP + layer * NEXP;
;     const f32x4* src = (const f32x4*)((tbl ? in[33] : in[32]) + (size_t)r * D) + lane;
; #pragma unroll
;     for (int j = 0; j < 16; ++j) v[j] = src[64 * j];
; }
; __device__ __forceinline__ void peer_row_store(const f32x4 (&v)[16], unsigned char* ws, int it, int layer, int lane) {
;     const int tbl = it >= NEXP, r = it - tbl * NEXP + layer * NEXP;
;     float am = 0.f;
; #pragma unroll
;     for (int j = 0; j < 16; ++j) am = fmaxf(fmaxf(am, fmaxf(fabsf(v[j][0]), fabsf(v[j][1]))), fmaxf(fabsf(v[j][2]), fabsf(v[j][3])));
;     ...
;     for (int it = it_lo + gw; it < it_hi; it += 2 * NGW) {
;         const int it1 = it + NGW, it2 = it + 2 * NGW;
;         peer_row_load(vb, in, it1 < it_hi ? it1 : it, only_layer, lane);
.LBB0_1490:
	s_add_i32 s19, s18, s3
	s_cmpk_lt_i32 s19, 0x3800
	s_cbranch_scc0 .LBB0_1496
.LBB0_1491:
	s_add_i32 s18, s19, s3
	s_cmpk_lt_i32 s18, 0x3800
	s_cselect_b64 s[6:7], -1, 0
	s_and_b64 s[8:9], s[6:7], exec
	s_cselect_b32 s8, s18, s19
	s_add_i32 s9, s8, 0x4000
	s_cmpk_gt_i32 s8, 0x3fff
	s_cselect_b32 s8, s8, s9
	s_cselect_b32 s10, s87, s85
	s_cselect_b32 s11, s86, s84
	s_ashr_i32 s9, s8, 31
	s_lshl_b64 s[8:9], s[8:9], 14
	s_add_u32 s8, s11, s8
	s_addc_u32 s9, s10, s9
	v_lshlrev_b32_e32 v132, 4, v130
	s_waitcnt vmcnt(32)
	v_lshl_add_u64 v[58:59], s[8:9], 0, v[132:133]
	v_add_co_u32_e32 v60, vcc, s14, v58
	global_load_dwordx4 v[122:125], v132, s[8:9] offset:1024
	global_load_dwordx4 v[118:121], v132, s[8:9] offset:2048
	v_addc_co_u32_e32 v61, vcc, 0, v59, vcc
	v_add_co_u32_e32 v66, vcc, s15, v58
	s_nop 1
	v_addc_co_u32_e32 v67, vcc, 0, v59, vcc
	global_load_dwordx4 v[114:117], v132, s[8:9] offset:3072
	global_load_dwordx4 v[110:113], v[66:67], off offset:-4096
	global_load_dwordx4 v[106:109], v[60:61], off offset:1024
	global_load_dwordx4 v[102:105], v[60:61], off offset:2048
	global_load_dwordx4 v[94:97], v[66:67], off
	global_load_dwordx4 v[90:93], v[66:67], off offset:1024
	global_load_dwordx4 v[82:85], v[66:67], off offset:2048
	global_load_dwordx4 v[78:81], v[66:67], off offset:3072
	v_add_co_u32_e32 v58, vcc, s16, v58
	s_nop 1
	v_addc_co_u32_e32 v59, vcc, 0, v59, vcc
	global_load_dwordx4 v[98:101], v[60:61], off offset:3072
	global_load_dwordx4 v[74:77], v[58:59], off
	global_load_dwordx4 v[70:73], v[58:59], off offset:1024
	global_load_dwordx4 v[66:69], v[58:59], off offset:2048
	global_load_dwordx4 v[126:129], v132, s[8:9]
	s_nop 0
	global_load_dwordx4 v[58:61], v[58:59], off offset:3072
	s_waitcnt vmcnt(17)
	v_max_f32_e64 v131, |v87|, |v87|
	v_max_f32_e64 v136, |v86|, |v86|
	v_max_f32_e32 v131, v136, v131
	v_max_f32_e64 v136, |v89|, |v89|
	v_max_f32_e64 v137, |v88|, |v88|
	v_max_f32_e32 v136, v137, v136
	v_max3_f32 v131, v131, 0, v136
	v_max_f32_e64 v136, |v63|, |v63|
	v_max_f32_e64 v137, |v62|, |v62|
	v_max_f32_e32 v136, v137, v136
	v_max_f32_e64 v137, |v65|, |v65|
	v_max_f32_e64 v138, |v64|, |v64|
	v_max_f32_e32 v137, v138, v137
	v_max3_f32 v131, v131, v136, v137
	v_max_f32_e64 v136, |v47|, |v47|
	v_max_f32_e64 v137, |v46|, |v46|
	v_max_f32_e32 v136, v137, v136
	v_max_f32_e64 v137, |v49|, |v49|
	v_max_f32_e64 v138, |v48|, |v48|
	v_max_f32_e32 v137, v138, v137
	v_max3_f32 v131, v131, v136, v137
	s_waitcnt vmcnt(28)
	v_max_f32_e64 v136, |v55|, |v55|
	v_max_f32_e64 v137, |v54|, |v54|
	v_max_f32_e32 v136, v137, v136
	v_max_f32_e64 v137, |v57|, |v57|
	v_max_f32_e64 v138, |v56|, |v56|
	v_max_f32_e32 v137, v138, v137
	v_max3_f32 v131, v131, v136, v137
	s_waitcnt vmcnt(27)
	v_max_f32_e64 v136, |v51|, |v51|
	v_max_f32_e64 v137, |v50|, |v50|
	v_max_f32_e32 v136, v137, v136
	v_max_f32_e64 v137, |v53|, |v53|
	v_max_f32_e64 v138, |v52|, |v52|
	v_max_f32_e32 v137, v138, v137
	v_max3_f32 v131, v131, v136, v137
	s_waitcnt vmcnt(26)
	v_max_f32_e64 v136, |v43|, |v43|
	v_max_f32_e64 v137, |v42|, |v42|
	v_max_f32_e32 v136, v137, v136
	v_max_f32_e64 v137, |v45|, |v45|
	v_max_f32_e64 v138, |v44|, |v44|
	v_max_f32_e32 v137, v138, v137
	v_max3_f32 v131, v131, v136, v137
	s_waitcnt vmcnt(25)
	v_max_f32_e64 v136, |v35|, |v35|
	v_max_f32_e64 v137, |v34|, |v34|
	v_max_f32_e32 v136, v137, v136
	v_max_f32_e64 v137, |v37|, |v37|
	v_max_f32_e64 v138, |v36|, |v36|
	v_max_f32_e32 v137, v138, v137
	v_max3_f32 v131, v131, v136, v137
	s_waitcnt vmcnt(24)
	v_max_f32_e64 v136, |v39|, |v39|
	v_max_f32_e64 v137, |v38|, |v38|
	v_max_f32_e32 v136, v137, v136
	v_max_f32_e64 v137, |v41|, |v41|
	v_max_f32_e64 v138, |v40|, |v40|
	v_max_f32_e32 v137, v138, v137
	v_max3_f32 v131, v131, v136, v137
	s_waitcnt vmcnt(23)
	v_max_f32_e64 v136, |v31|, |v31|
	v_max_f32_e64 v137, |v30|, |v30|
	v_max_f32_e32 v136, v137, v136
	v_max_f32_e64 v137, |v33|, |v33|
	v_max_f32_e64 v138, |v32|, |v32|
	v_max_f32_e32 v137, v138, v137
	v_max3_f32 v131, v131, v136, v137
	s_waitcnt vmcnt(22)
	v_max_f32_e64 v136, |v27|, |v27|
	v_max_f32_e64 v137, |v26|, |v26|
	v_max_f32_e32 v136, v137, v136
	v_max_f32_e64 v137, |v29|, |v29|
	v_max_f32_e64 v138, |v28|, |v28|
	v_max_f32_e32 v137, v138, v137
	v_max3_f32 v131, v131, v136, v137
	s_waitcnt vmcnt(21)
	v_max_f32_e64 v136, |v23|, |v23|
	v_max_f32_e64 v137, |v22|, |v22|
	v_max_f32_e32 v136, v137, v136
	v_max_f32_e64 v137, |v25|, |v25|
	v_max_f32_e64 v138, |v24|, |v24|
	v_max_f32_e32 v137, v138, v137
	v_max3_f32 v131, v131, v136, v137
	s_waitcnt vmcnt(20)
	v_max_f32_e64 v136, |v15|, |v15|
	v_max_f32_e64 v137, |v14|, |v14|
	v_max_f32_e32 v136, v137, v136
	v_max_f32_e64 v137, |v17|, |v17|
	v_max_f32_e64 v138, |v16|, |v16|
	v_max_f32_e32 v137, v138, v137
	v_max3_f32 v131, v131, v136, v137
	s_waitcnt vmcnt(19)
	v_max_f32_e64 v136, |v19|, |v19|
	v_max_f32_e64 v137, |v18|, |v18|
	v_max_f32_e32 v136, v137, v136
	v_max_f32_e64 v137, |v21|, |v21|
	v_max_f32_e64 v138, |v20|, |v20|
	v_max_f32_e32 v137, v138, v137
	v_max3_f32 v131, v131, v136, v137
	s_waitcnt vmcnt(18)
	v_max_f32_e64 v136, |v11|, |v11|
	v_max_f32_e64 v137, |v10|, |v10|
	v_max_f32_e32 v136, v137, v136
	v_max_f32_e64 v137, |v13|, |v13|
	v_max_f32_e64 v138, |v12|, |v12|
	v_max_f32_e32 v137, v138, v137
	v_max3_f32 v131, v131, v136, v137
	s_waitcnt vmcnt(17)
	v_max_f32_e64 v136, |v7|, |v7|
	v_max_f32_e64 v137, |v6|, |v6|
	v_max_f32_e32 v136, v137, v136
	v_max_f32_e64 v137, |v9|, |v9|
	v_max_f32_e64 v138, |v8|, |v8|
	v_max_f32_e32 v137, v138, v137
	v_max3_f32 v131, v131, v136, v137
	s_waitcnt vmcnt(16)
; template <int CTRL> __device__ __forceinline__ unsigned dppu(unsigned x) { return (unsigned)__builtin_amdgcn_mov_dpp((int)x, CTRL, 0xf, 0xf, true); }
; __device__ __forceinline__ unsigned max64u(unsigned x) {
;     x = umax_u(x, dppu<DPP_XOR1>(x)); x = umax_u(x, dppu<DPP_XOR2>(x)); x = umax_u(x, dppu<DPP_HMIRROR>(x)); x = umax_u(x, dppu<DPP_MIRROR>(x));
;     auto s = __builtin_amdgcn_permlane16_swap(x, x, false, false); x = umax_u(s[0], s[1]);
;     auto t = __builtin_amdgcn_permlane32_swap(x, x, false, false); return umax_u(t[0], t[1]);
; }
; __device__ __forceinline__ void peer_row_store(const f32x4 (&v)[16], unsigned char* ws, int it, int layer, int lane) {
;     const int tbl = it >= NEXP, r = it - tbl * NEXP + layer * NEXP;
;     float am = 0.f;
; #pragma unroll
;     for (int j = 0; j < 16; ++j) am = fmaxf(fmaxf(am, fmaxf(fabsf(v[j][0]), fabsf(v[j][1]))), fmaxf(fabsf(v[j][2]), fabsf(v[j][3])));
;     am = __uint_as_float(max64u(__float_as_uint(am)));
;     const float q = am > 0.f ? 256.0f / am : 0.f;
;     unsigned* dst = (unsigned*)(ws + (tbl ? WS_PV : WS_PU) + (size_t)r * D) + lane;
;     if (tbl) {
;         const int rl = it - NEXP;
;         unsigned char* pvl = ws + WS_PV + (size_t)layer * NEXP * D + (size_t)rl * 8 + (lane & 1) * 4;
;         unsigned char* pvg = ws + WS_PV + (size_t)layer * NEXP * D + (size_t)NEXP * 2048 + (size_t)rl * 2048 + 4 * lane;
; #pragma unroll
;         for (int j = 0; j < 16; ++j) { int w = __builtin_amdgcn_cvt_pk_bf8_f32(v[j][0] * q, v[j][1] * q, 0, false); w = __builtin_amdgcn_cvt_pk_bf8_f32(v[j][2] * q, v[j][3] * q, w, true);
;             if (j < 8) *(unsigned*)(pvl + (size_t)((lane >> 1) + 32 * j) * (NEXP * 8)) = (unsigned)w;
;             else *(unsigned*)(pvg + 256 * (j - 8)) = (unsigned)w; }
;     } else {
; #pragma unroll
;         for (int j = 0; j < 16; ++j) { int w = __builtin_amdgcn_cvt_pk_fp8_f32(v[j][0] * q, v[j][1] * q, 0, false); w = __builtin_amdgcn_cvt_pk_fp8_f32(v[j][2] * q, v[j][3] * q, w, true); dst[64 * j] = (unsigned)w; }
;     }
;     if (lane == 0) ((float*)(ws + (tbl ? WS_SV : WS_SU)))[r] = am * (1.0f / 256.0f);
; }
	v_max_f32_e64 v136, |v3|, |v3|
	v_max_f32_e64 v137, |v2|, |v2|
	v_max_f32_e32 v136, v137, v136
	v_max_f32_e64 v137, |v5|, |v5|
	v_max_f32_e64 v138, |v4|, |v4|
	v_max_f32_e32 v137, v138, v137
	v_max3_f32 v131, v131, v136, v137
	s_nop 1
	v_max_u32_dpp v131, v131, v131 quad_perm:[1,0,3,2] row_mask:0xf bank_mask:0xf bound_ctrl:1
	s_nop 1
	v_max_u32_dpp v131, v131, v131 quad_perm:[2,3,0,1] row_mask:0xf bank_mask:0xf bound_ctrl:1
	s_nop 1
	v_max_u32_dpp v131, v131, v131 row_half_mirror row_mask:0xf bank_mask:0xf bound_ctrl:1
	s_nop 1
	v_max_u32_dpp v131, v131, v131 row_mirror row_mask:0xf bank_mask:0xf bound_ctrl:1
	v_mov_b32_e32 v136, v131
	s_nop 1
	v_permlane16_swap_b32_e32 v131, v136
	v_max_u32_e32 v131, v131, v136
	v_mov_b32_e32 v136, v131
	s_nop 1
	v_permlane32_swap_b32_e32 v131, v136
	v_max_u32_e32 v131, v131, v136
	v_div_scale_f32 v136, s[8:9], v131, v131, s17
	v_rcp_f32_e32 v137, v136
	s_add_i32 s8, s19, 0x4000
	s_ashr_i32 s9, s8, 31
	s_lshl_b64 s[10:11], s[8:9], 12
	v_fma_f32 v138, -v136, v137, 1.0
	v_fmac_f32_e32 v137, v138, v137
	v_div_scale_f32 v138, vcc, s17, v131, s17
	v_mul_f32_e32 v139, v138, v137
	v_fma_f32 v140, -v136, v139, v138
	v_fmac_f32_e32 v139, v140, v137
	v_fma_f32 v136, -v136, v139, v138
	v_div_fmas_f32 v136, v136, v137, v139
	v_div_fixup_f32 v136, v136, v131, s17
	v_cmp_lt_f32_e32 vcc, 0, v131
	v_mov_b32_e32 v139, v133
	s_nop 0
	v_cndmask_b32_e32 v138, 0, v136, vcc
	v_mul_f32_e32 v86, v86, v138
	v_mul_f32_e32 v87, v87, v138
	v_cvt_pk_fp8_f32 v139, v86, v87
	v_mul_f32_e32 v86, v88, v138
	v_mul_f32_e32 v62, v62, v138
	v_mul_f32_e32 v63, v63, v138
	v_mov_b32_e32 v88, v133
	v_cvt_pk_fp8_f32 v88, v62, v63
	v_mul_f32_e32 v62, v64, v138
	v_mul_f32_e32 v63, v65, v138
	v_mul_f32_e32 v46, v46, v138
	v_cvt_pk_fp8_f32 v88, v62, v63 op_sel:[0,0,1]
	v_mul_f32_e32 v47, v47, v138
	v_mov_b32_e32 v62, v133
	v_cvt_pk_fp8_f32 v62, v46, v47
	v_mul_f32_e32 v46, v48, v138
	v_mul_f32_e32 v47, v49, v138
	v_mul_f32_e32 v48, v54, v138
	v_mul_f32_e32 v49, v55, v138
	v_mov_b32_e32 v54, v133
	v_cvt_pk_fp8_f32 v54, v48, v49
	v_mul_f32_e32 v42, v42, v138
	v_mul_f32_e32 v43, v43, v138
	v_mov_b32_e32 v49, v133
	v_cvt_pk_fp8_f32 v49, v42, v43
	v_mul_f32_e32 v42, v44, v138
	v_mul_f32_e32 v43, v45, v138
	v_mul_f32_e32 v34, v34, v138
	v_cvt_pk_fp8_f32 v49, v42, v43 op_sel:[0,0,1]
	v_mul_f32_e32 v35, v35, v138
	v_mov_b32_e32 v42, v133
	v_cvt_pk_fp8_f32 v42, v34, v35
	v_mul_f32_e32 v34, v36, v138
	v_mul_f32_e32 v35, v37, v138
	v_mul_f32_e32 v36, v38, v138
	v_mul_f32_e32 v37, v39, v138
	v_mov_b32_e32 v38, v133
	v_cvt_pk_fp8_f32 v38, v36, v37
	v_cvt_pk_fp8_f32 v42, v34, v35 op_sel:[0,0,1]
	v_mul_f32_e32 v34, v40, v138
	v_mul_f32_e32 v35, v41, v138
	v_cvt_pk_fp8_f32 v38, v34, v35 op_sel:[0,0,1]
	v_mul_f32_e32 v30, v30, v138
	v_mul_f32_e32 v31, v31, v138
	v_mov_b32_e32 v34, v133
	v_cvt_pk_fp8_f32 v34, v30, v31
	v_mul_f32_e32 v30, v32, v138
	v_mul_f32_e32 v26, v26, v138
	v_mul_f32_e32 v27, v27, v138
	v_mov_b32_e32 v32, v133
	v_cvt_pk_fp8_f32 v32, v26, v27
	v_mul_f32_e32 v26, v28, v138
	v_mul_f32_e32 v27, v29, v138
	v_mul_f32_e32 v22, v22, v138
	v_cvt_pk_fp8_f32 v32, v26, v27 op_sel:[0,0,1]
	v_mul_f32_e32 v23, v23, v138
	v_mov_b32_e32 v26, v133
	v_cvt_pk_fp8_f32 v26, v22, v23
	v_mul_f32_e32 v22, v24, v138
	v_mul_f32_e32 v14, v14, v138
	v_mul_f32_e32 v15, v15, v138
	v_mov_b32_e32 v24, v133
	v_cvt_pk_fp8_f32 v24, v14, v15
	v_mul_f32_e32 v15, v17, v138
	v_mul_f32_e32 v10, v10, v138
	v_mul_f32_e32 v11, v11, v138
	v_mov_b32_e32 v17, v133
	v_cvt_pk_fp8_f32 v17, v10, v11
	v_cvt_pk_fp8_f32 v62, v46, v47 op_sel:[0,0,1]
	v_mul_f32_e32 v46, v56, v138
	v_mul_f32_e32 v47, v57, v138
	v_mul_f32_e32 v14, v16, v138
	v_cvt_pk_fp8_f32 v54, v46, v47 op_sel:[0,0,1]
	v_mul_f32_e32 v46, v50, v138
	v_mul_f32_e32 v47, v51, v138
	v_mov_b32_e32 v48, v133
	v_cvt_pk_fp8_f32 v24, v14, v15 op_sel:[0,0,1]
	v_mul_f32_e32 v14, v18, v138
	v_mul_f32_e32 v15, v19, v138
	v_mov_b32_e32 v16, v133
	v_cvt_pk_fp8_f32 v48, v46, v47
	v_cvt_pk_fp8_f32 v16, v14, v15
	v_mul_f32_e32 v10, v12, v138
	v_mul_f32_e32 v11, v13, v138
	v_cvt_pk_fp8_f32 v17, v10, v11 op_sel:[0,0,1]
	v_mul_f32_e32 v6, v6, v138
	v_mul_f32_e32 v7, v7, v138
	v_mov_b32_e32 v10, v133
	v_cvt_pk_fp8_f32 v10, v6, v7
	v_mul_f32_e32 v6, v8, v138
	v_mul_f32_e32 v2, v2, v138
	v_mul_f32_e32 v3, v3, v138
	v_mov_b32_e32 v8, v133
	v_mul_f32_e32 v87, v89, v138
	v_mul_f32_e32 v46, v52, v138
	v_mul_f32_e32 v47, v53, v138
	v_mul_f32_e32 v31, v33, v138
	v_mul_f32_e32 v14, v20, v138
	v_mul_f32_e32 v15, v21, v138
	v_cvt_pk_fp8_f32 v8, v2, v3
	v_cvt_pk_fp8_f32 v139, v86, v87 op_sel:[0,0,1]
	v_cvt_pk_fp8_f32 v48, v46, v47 op_sel:[0,0,1]
	v_cvt_pk_fp8_f32 v34, v30, v31 op_sel:[0,0,1]
	v_cvt_pk_fp8_f32 v16, v14, v15 op_sel:[0,0,1]
	v_mul_f32_e32 v23, v25, v138
	v_mul_f32_e32 v7, v9, v138
	v_cvt_pk_fp8_f32 v26, v22, v23 op_sel:[0,0,1]
	v_cvt_pk_fp8_f32 v10, v6, v7 op_sel:[0,0,1]
	v_mul_f32_e32 v2, v4, v138
	v_mul_f32_e32 v3, v5, v138
	v_lshl_add_u64 v[136:137], v[134:135], 0, s[10:11]
	v_cvt_pk_fp8_f32 v8, v2, v3 op_sel:[0,0,1]
	global_store_dword v[136:137], v139, off
	global_store_dword v[136:137], v88, off offset:256
	global_store_dword v[136:137], v62, off offset:512
	global_store_dword v[136:137], v54, off offset:768
	global_store_dword v[136:137], v48, off offset:1024
	global_store_dword v[136:137], v49, off offset:1280
	global_store_dword v[136:137], v42, off offset:1536
	global_store_dword v[136:137], v38, off offset:1792
	global_store_dword v[136:137], v34, off offset:2048
	global_store_dword v[136:137], v32, off offset:2304
	global_store_dword v[136:137], v26, off offset:2560
	global_store_dword v[136:137], v24, off offset:2816
	global_store_dword v[136:137], v16, off offset:3072
	global_store_dword v[136:137], v17, off offset:3328
	global_store_dword v[136:137], v10, off offset:3584
	global_store_dword v[136:137], v8, off offset:3840
	s_and_saveexec_b64 s[10:11], s[0:1]
	s_cbranch_execz .LBB0_1493
	s_lshl_b64 s[8:9], s[8:9], 2
	s_add_u32 s8, s5, s8
	s_addc_u32 s9, s12, s9
	v_mul_f32_e32 v2, 0x3b800000, v131
	global_store_dword v133, v2, s[8:9]
; __device__ __forceinline__ void peer_row_load(f32x4 (&v)[16], const float* const (&in)[34], int it, int layer, int lane) {
;     const int tbl = it >= NEXP, r = it - tbl * NEXP + layer * NEXP;
;     const f32x4* src = (const f32x4*)((tbl ? in[33] : in[32]) + (size_t)r * D) + lane;
; #pragma unroll
;     for (int j = 0; j < 16; ++j) v[j] = src[64 * j];
; }
; __device__ __forceinline__ void peer_row_store(const f32x4 (&v)[16], unsigned char* ws, int it, int layer, int lane) {
;     const int tbl = it >= NEXP, r = it - tbl * NEXP + layer * NEXP;
;     float am = 0.f;
; #pragma unroll
;     for (int j = 0; j < 16; ++j) am = fmaxf(fmaxf(am, fmaxf(fabsf(v[j][0]), fabsf(v[j][1]))), fmaxf(fabsf(v[j][2]), fabsf(v[j][3])));
;     ...
;         peer_row_load(va, in, it2 < it_hi ? it2 : it, only_layer, lane);
;         __builtin_amdgcn_sched_barrier(0);
;         if (it1 < it_hi) peer_row_store(vb, ws, it1, only_layer, lane);
.LBB0_1493:
	s_or_b64 exec, exec, s[10:11]
	s_add_i32 s8, s13, s19
	s_cmpk_lt_i32 s8, 0x3800
	s_cselect_b32 s8, s8, s19
	s_add_i32 s9, s8, 0x4000
	s_cmpk_gt_i32 s8, 0x3fff
	s_cselect_b32 s8, s8, s9
	s_cselect_b32 s10, s87, s85
	s_cselect_b32 s11, s86, s84
	s_ashr_i32 s9, s8, 31
	s_lshl_b64 s[8:9], s[8:9], 14
	s_add_u32 s8, s11, s8
	s_addc_u32 s9, s10, s9
	v_lshl_add_u64 v[2:3], s[8:9], 0, v[132:133]
	v_add_co_u32_e32 v4, vcc, s14, v2
	global_load_dwordx4 v[62:65], v132, s[8:9] offset:1024
	global_load_dwordx4 v[46:49], v132, s[8:9] offset:2048
	v_addc_co_u32_e32 v5, vcc, 0, v3, vcc
	v_add_co_u32_e32 v6, vcc, s15, v2
	s_nop 1
	v_addc_co_u32_e32 v7, vcc, 0, v3, vcc
	global_load_dwordx4 v[54:57], v132, s[8:9] offset:3072
	global_load_dwordx4 v[50:53], v[6:7], off offset:-4096
	global_load_dwordx4 v[42:45], v[4:5], off offset:1024
	global_load_dwordx4 v[34:37], v[4:5], off offset:2048
	global_load_dwordx4 v[30:33], v[6:7], off
	global_load_dwordx4 v[26:29], v[6:7], off offset:1024
	global_load_dwordx4 v[22:25], v[6:7], off offset:2048
	global_load_dwordx4 v[14:17], v[6:7], off offset:3072
	v_add_co_u32_e32 v2, vcc, 0x3000, v2
	s_nop 1
	v_addc_co_u32_e32 v3, vcc, 0, v3, vcc
	global_load_dwordx4 v[38:41], v[4:5], off offset:3072
	global_load_dwordx4 v[18:21], v[2:3], off
	global_load_dwordx4 v[10:13], v[2:3], off offset:1024
	global_load_dwordx4 v[6:9], v[2:3], off offset:2048
	global_load_dwordx4 v[86:89], v132, s[8:9]
	s_nop 0
	global_load_dwordx4 v[2:5], v[2:3], off offset:3072
	s_andn2_b64 vcc, exec, s[6:7]
	s_cbranch_vccnz .LBB0_1490
	s_waitcnt vmcnt(33)
	v_max_f32_e64 v131, |v127|, |v127|
	v_max_f32_e64 v132, |v126|, |v126|
	v_max_f32_e32 v131, v132, v131
	v_max_f32_e64 v132, |v129|, |v129|
	v_max_f32_e64 v136, |v128|, |v128|
	v_max_f32_e32 v132, v136, v132
	v_max3_f32 v131, v131, 0, v132
	v_max_f32_e64 v132, |v123|, |v123|
	v_max_f32_e64 v136, |v122|, |v122|
	v_max_f32_e32 v132, v136, v132
	v_max_f32_e64 v136, |v125|, |v125|
	v_max_f32_e64 v137, |v124|, |v124|
	v_max_f32_e32 v136, v137, v136
	v_max3_f32 v131, v131, v132, v136
	v_max_f32_e64 v132, |v119|, |v119|
	v_max_f32_e64 v136, |v118|, |v118|
	v_max_f32_e32 v132, v136, v132
	v_max_f32_e64 v136, |v121|, |v121|
	v_max_f32_e64 v137, |v120|, |v120|
	v_max_f32_e32 v136, v137, v136
	v_max3_f32 v131, v131, v132, v136
	v_max_f32_e64 v132, |v115|, |v115|
	v_max_f32_e64 v136, |v114|, |v114|
	v_max_f32_e32 v132, v136, v132
	v_max_f32_e64 v136, |v117|, |v117|
	v_max_f32_e64 v137, |v116|, |v116|
	v_max_f32_e32 v136, v137, v136
	v_max3_f32 v131, v131, v132, v136
	v_max_f32_e64 v132, |v111|, |v111|
	v_max_f32_e64 v136, |v110|, |v110|
	v_max_f32_e32 v132, v136, v132
	v_max_f32_e64 v136, |v113|, |v113|
	v_max_f32_e64 v137, |v112|, |v112|
	v_max_f32_e32 v136, v137, v136
	v_max3_f32 v131, v131, v132, v136
	v_max_f32_e64 v132, |v107|, |v107|
	v_max_f32_e64 v136, |v106|, |v106|
	v_max_f32_e32 v132, v136, v132
	v_max_f32_e64 v136, |v109|, |v109|
	v_max_f32_e64 v137, |v108|, |v108|
	v_max_f32_e32 v136, v137, v136
	v_max3_f32 v131, v131, v132, v136
	v_max_f32_e64 v132, |v103|, |v103|
	v_max_f32_e64 v136, |v102|, |v102|
	v_max_f32_e32 v132, v136, v132
	v_max_f32_e64 v136, |v105|, |v105|
	v_max_f32_e64 v137, |v104|, |v104|
	v_max_f32_e32 v136, v137, v136
	v_max3_f32 v131, v131, v132, v136
	v_max_f32_e64 v132, |v99|, |v99|
	v_max_f32_e64 v136, |v98|, |v98|
	v_max_f32_e32 v132, v136, v132
	v_max_f32_e64 v136, |v101|, |v101|
	v_max_f32_e64 v137, |v100|, |v100|
	v_max_f32_e32 v136, v137, v136
	v_max3_f32 v131, v131, v132, v136
	v_max_f32_e64 v132, |v95|, |v95|
	v_max_f32_e64 v136, |v94|, |v94|
	v_max_f32_e32 v132, v136, v132
	v_max_f32_e64 v136, |v97|, |v97|
	v_max_f32_e64 v137, |v96|, |v96|
	v_max_f32_e32 v136, v137, v136
	v_max3_f32 v131, v131, v132, v136
	v_max_f32_e64 v132, |v91|, |v91|
	v_max_f32_e64 v136, |v90|, |v90|
	v_max_f32_e32 v132, v136, v132
	v_max_f32_e64 v136, |v93|, |v93|
	v_max_f32_e64 v137, |v92|, |v92|
	v_max_f32_e32 v136, v137, v136
	v_max3_f32 v131, v131, v132, v136
	v_max_f32_e64 v132, |v83|, |v83|
	v_max_f32_e64 v136, |v82|, |v82|
	v_max_f32_e32 v132, v136, v132
	v_max_f32_e64 v136, |v85|, |v85|
	v_max_f32_e64 v137, |v84|, |v84|
	v_max_f32_e32 v136, v137, v136
	v_max3_f32 v131, v131, v132, v136
	v_max_f32_e64 v132, |v79|, |v79|
	v_max_f32_e64 v136, |v78|, |v78|
	v_max_f32_e32 v132, v136, v132
	v_max_f32_e64 v136, |v81|, |v81|
	v_max_f32_e64 v137, |v80|, |v80|
	v_max_f32_e32 v136, v137, v136
	v_max3_f32 v131, v131, v132, v136
	v_max_f32_e64 v132, |v75|, |v75|
	v_max_f32_e64 v136, |v74|, |v74|
	v_max_f32_e32 v132, v136, v132
	v_max_f32_e64 v136, |v77|, |v77|
	v_max_f32_e64 v137, |v76|, |v76|
	v_max_f32_e32 v136, v137, v136
	v_max3_f32 v131, v131, v132, v136
	v_max_f32_e64 v132, |v71|, |v71|
	v_max_f32_e64 v136, |v70|, |v70|
	v_max_f32_e32 v132, v136, v132
	v_max_f32_e64 v136, |v73|, |v73|
	v_max_f32_e64 v137, |v72|, |v72|
	v_max_f32_e32 v136, v137, v136
	v_max3_f32 v131, v131, v132, v136
	v_max_f32_e64 v132, |v67|, |v67|
	v_max_f32_e64 v136, |v66|, |v66|
	v_max_f32_e32 v132, v136, v132
	v_max_f32_e64 v136, |v69|, |v69|
	v_max_f32_e64 v137, |v68|, |v68|
	v_max_f32_e32 v136, v137, v136
	v_max3_f32 v131, v131, v132, v136
	s_waitcnt vmcnt(32)
; template <int CTRL> __device__ __forceinline__ unsigned dppu(unsigned x) { return (unsigned)__builtin_amdgcn_mov_dpp((int)x, CTRL, 0xf, 0xf, true); }
; __device__ __forceinline__ unsigned max64u(unsigned x) {
;     x = umax_u(x, dppu<DPP_XOR1>(x)); x = umax_u(x, dppu<DPP_XOR2>(x)); x = umax_u(x, dppu<DPP_HMIRROR>(x)); x = umax_u(x, dppu<DPP_MIRROR>(x));
;     auto s = __builtin_amdgcn_permlane16_swap(x, x, false, false); x = umax_u(s[0], s[1]);
;     auto t = __builtin_amdgcn_permlane32_swap(x, x, false, false); return umax_u(t[0], t[1]);
; }
; __device__ __forceinline__ void peer_row_store(const f32x4 (&v)[16], unsigned char* ws, int it, int layer, int lane) {
;     const int tbl = it >= NEXP, r = it - tbl * NEXP + layer * NEXP;
;     float am = 0.f;
; #pragma unroll
;     for (int j = 0; j < 16; ++j) am = fmaxf(fmaxf(am, fmaxf(fabsf(v[j][0]), fabsf(v[j][1]))), fmaxf(fabsf(v[j][2]), fabsf(v[j][3])));
;     am = __uint_as_float(max64u(__float_as_uint(am)));
;     const float q = am > 0.f ? 256.0f / am : 0.f;
;     unsigned* dst = (unsigned*)(ws + (tbl ? WS_PV : WS_PU) + (size_t)r * D) + lane;
;     if (tbl) {
;         const int rl = it - NEXP;
;         unsigned char* pvl = ws + WS_PV + (size_t)layer * NEXP * D + (size_t)rl * 8 + (lane & 1) * 4;
;         unsigned char* pvg = ws + WS_PV + (size_t)layer * NEXP * D + (size_t)NEXP * 2048 + (size_t)rl * 2048 + 4 * lane;
; #pragma unroll
;         for (int j = 0; j < 16; ++j) { int w = __builtin_amdgcn_cvt_pk_bf8_f32(v[j][0] * q, v[j][1] * q, 0, false); w = __builtin_amdgcn_cvt_pk_bf8_f32(v[j][2] * q, v[j][3] * q, w, true);
;             if (j < 8) *(unsigned*)(pvl + (size_t)((lane >> 1) + 32 * j) * (NEXP * 8)) = (unsigned)w;
;             else *(unsigned*)(pvg + 256 * (j - 8)) = (unsigned)w; }
;     } else {
; #pragma unroll
;         for (int j = 0; j < 16; ++j) { int w = __builtin_amdgcn_cvt_pk_fp8_f32(v[j][0] * q, v[j][1] * q, 0, false); w = __builtin_amdgcn_cvt_pk_fp8_f32(v[j][2] * q, v[j][3] * q, w, true); dst[64 * j] = (unsigned)w; }
;     }
;     if (lane == 0) ((float*)(ws + (tbl ? WS_SV : WS_SU)))[r] = am * (1.0f / 256.0f);
; }
	v_max_f32_e64 v132, |v59|, |v59|
	v_max_f32_e64 v136, |v58|, |v58|
	v_max_f32_e32 v132, v136, v132
	v_max_f32_e64 v136, |v61|, |v61|
	v_max_f32_e64 v137, |v60|, |v60|
	v_max_f32_e32 v136, v137, v136
	v_max3_f32 v131, v131, v132, v136
	s_nop 1
	v_max_u32_dpp v131, v131, v131 quad_perm:[1,0,3,2] row_mask:0xf bank_mask:0xf bound_ctrl:1
	s_nop 1
	v_max_u32_dpp v131, v131, v131 quad_perm:[2,3,0,1] row_mask:0xf bank_mask:0xf bound_ctrl:1
	s_nop 1
	v_max_u32_dpp v131, v131, v131 row_half_mirror row_mask:0xf bank_mask:0xf bound_ctrl:1
	s_nop 1
	v_max_u32_dpp v131, v131, v131 row_mirror row_mask:0xf bank_mask:0xf bound_ctrl:1
	v_mov_b32_e32 v132, v131
	s_nop 1
	v_permlane16_swap_b32_e32 v131, v132
	v_max_u32_e32 v131, v131, v132
	v_mov_b32_e32 v132, v131
	s_nop 1
	v_permlane32_swap_b32_e32 v131, v132
	v_max_u32_e32 v131, v131, v132
	v_div_scale_f32 v132, s[6:7], v131, v131, s17
	v_rcp_f32_e32 v136, v132
	s_add_i32 s6, s18, 0x4000
	s_ashr_i32 s7, s6, 31
	s_lshl_b64 s[8:9], s[6:7], 12
	v_fma_f32 v137, -v132, v136, 1.0
	v_fmac_f32_e32 v136, v137, v136
	v_div_scale_f32 v137, vcc, s17, v131, s17
	v_mul_f32_e32 v138, v137, v136
	v_fma_f32 v139, -v132, v138, v137
	v_fmac_f32_e32 v138, v139, v136
	v_fma_f32 v132, -v132, v138, v137
	v_div_fmas_f32 v132, v132, v136, v138
	v_div_fixup_f32 v132, v132, v131, s17
	v_cmp_lt_f32_e32 vcc, 0, v131
	v_mov_b32_e32 v138, v133
	v_lshl_add_u64 v[136:137], v[134:135], 0, s[8:9]
	v_cndmask_b32_e32 v132, 0, v132, vcc
	v_mul_f32_e32 v126, v126, v132
	v_mul_f32_e32 v127, v127, v132
	v_cvt_pk_fp8_f32 v138, v126, v127
	v_mul_f32_e32 v126, v128, v132
	v_mul_f32_e32 v122, v122, v132
	v_mul_f32_e32 v123, v123, v132
	v_mov_b32_e32 v128, v133
	v_cvt_pk_fp8_f32 v128, v122, v123
	v_mul_f32_e32 v122, v124, v132
	v_mul_f32_e32 v123, v125, v132
	v_mul_f32_e32 v118, v118, v132
	v_cvt_pk_fp8_f32 v128, v122, v123 op_sel:[0,0,1]
	v_mul_f32_e32 v119, v119, v132
	v_mov_b32_e32 v122, v133
	v_cvt_pk_fp8_f32 v122, v118, v119
	v_mul_f32_e32 v118, v120, v132
	v_mul_f32_e32 v114, v114, v132
	v_mul_f32_e32 v115, v115, v132
	v_mov_b32_e32 v120, v133
	v_cvt_pk_fp8_f32 v120, v114, v115
	v_mul_f32_e32 v114, v116, v132
	v_mul_f32_e32 v115, v117, v132
	v_mul_f32_e32 v110, v110, v132
	v_cvt_pk_fp8_f32 v120, v114, v115 op_sel:[0,0,1]
	v_mul_f32_e32 v111, v111, v132
	v_mov_b32_e32 v114, v133
	v_cvt_pk_fp8_f32 v114, v110, v111
	v_mul_f32_e32 v110, v112, v132
	v_mul_f32_e32 v106, v106, v132
	v_mul_f32_e32 v107, v107, v132
	v_mov_b32_e32 v112, v133
	v_cvt_pk_fp8_f32 v112, v106, v107
	v_mul_f32_e32 v106, v108, v132
	v_mul_f32_e32 v107, v109, v132
	v_mul_f32_e32 v102, v102, v132
	v_cvt_pk_fp8_f32 v112, v106, v107 op_sel:[0,0,1]
	v_mul_f32_e32 v103, v103, v132
	v_mov_b32_e32 v106, v133
	v_cvt_pk_fp8_f32 v106, v102, v103
	v_mul_f32_e32 v102, v104, v132
	v_mul_f32_e32 v98, v98, v132
	v_mul_f32_e32 v99, v99, v132
	v_mov_b32_e32 v104, v133
	v_cvt_pk_fp8_f32 v104, v98, v99
	v_mul_f32_e32 v98, v100, v132
	v_mul_f32_e32 v99, v101, v132
	v_mul_f32_e32 v94, v94, v132
	v_cvt_pk_fp8_f32 v104, v98, v99 op_sel:[0,0,1]
	v_mul_f32_e32 v95, v95, v132
	v_mov_b32_e32 v98, v133
	v_cvt_pk_fp8_f32 v98, v94, v95
	v_mul_f32_e32 v94, v96, v132
	v_mul_f32_e32 v90, v90, v132
	v_mul_f32_e32 v91, v91, v132
	v_mov_b32_e32 v96, v133
	v_cvt_pk_fp8_f32 v96, v90, v91
	v_mul_f32_e32 v90, v92, v132
	v_mul_f32_e32 v91, v93, v132
	v_mul_f32_e32 v82, v82, v132
	v_cvt_pk_fp8_f32 v96, v90, v91 op_sel:[0,0,1]
	v_mul_f32_e32 v83, v83, v132
	v_mov_b32_e32 v90, v133
	v_cvt_pk_fp8_f32 v90, v82, v83
	v_mul_f32_e32 v82, v84, v132
	v_mul_f32_e32 v78, v78, v132
	v_mul_f32_e32 v79, v79, v132
	v_mov_b32_e32 v84, v133
	v_cvt_pk_fp8_f32 v84, v78, v79
	v_mul_f32_e32 v78, v80, v132
	v_mul_f32_e32 v79, v81, v132
	v_mul_f32_e32 v74, v74, v132
	v_cvt_pk_fp8_f32 v84, v78, v79 op_sel:[0,0,1]
	v_mul_f32_e32 v75, v75, v132
	v_mov_b32_e32 v78, v133
	v_cvt_pk_fp8_f32 v78, v74, v75
	v_mul_f32_e32 v74, v76, v132
	v_mul_f32_e32 v70, v70, v132
	v_mul_f32_e32 v71, v71, v132
	v_mov_b32_e32 v76, v133
	v_cvt_pk_fp8_f32 v76, v70, v71
	v_mul_f32_e32 v70, v72, v132
	v_mul_f32_e32 v71, v73, v132
	v_mul_f32_e32 v66, v66, v132
	v_cvt_pk_fp8_f32 v76, v70, v71 op_sel:[0,0,1]
	v_mul_f32_e32 v67, v67, v132
	v_mov_b32_e32 v70, v133
	v_cvt_pk_fp8_f32 v70, v66, v67
	v_mul_f32_e32 v66, v68, v132
	v_mul_f32_e32 v58, v58, v132
	v_mul_f32_e32 v59, v59, v132
	v_mov_b32_e32 v68, v133
	v_mul_f32_e32 v127, v129, v132
	v_mul_f32_e32 v111, v113, v132
	v_mul_f32_e32 v95, v97, v132
	v_mul_f32_e32 v75, v77, v132
	v_cvt_pk_fp8_f32 v68, v58, v59
	v_cvt_pk_fp8_f32 v138, v126, v127 op_sel:[0,0,1]
	v_cvt_pk_fp8_f32 v114, v110, v111 op_sel:[0,0,1]
	v_cvt_pk_fp8_f32 v98, v94, v95 op_sel:[0,0,1]
	v_cvt_pk_fp8_f32 v78, v74, v75 op_sel:[0,0,1]
	v_mul_f32_e32 v119, v121, v132
	v_mul_f32_e32 v103, v105, v132
	v_mul_f32_e32 v83, v85, v132
	v_mul_f32_e32 v67, v69, v132
	v_cvt_pk_fp8_f32 v122, v118, v119 op_sel:[0,0,1]
	v_cvt_pk_fp8_f32 v106, v102, v103 op_sel:[0,0,1]
	v_cvt_pk_fp8_f32 v90, v82, v83 op_sel:[0,0,1]
	v_cvt_pk_fp8_f32 v70, v66, v67 op_sel:[0,0,1]
	v_mul_f32_e32 v58, v60, v132
	v_mul_f32_e32 v59, v61, v132
	v_cvt_pk_fp8_f32 v68, v58, v59 op_sel:[0,0,1]
	global_store_dword v[136:137], v138, off
	global_store_dword v[136:137], v128, off offset:256
	global_store_dword v[136:137], v122, off offset:512
	global_store_dword v[136:137], v120, off offset:768
	global_store_dword v[136:137], v114, off offset:1024
	global_store_dword v[136:137], v112, off offset:1280
	global_store_dword v[136:137], v106, off offset:1536
	global_store_dword v[136:137], v104, off offset:1792
	global_store_dword v[136:137], v98, off offset:2048
	global_store_dword v[136:137], v96, off offset:2304
	global_store_dword v[136:137], v90, off offset:2560
	global_store_dword v[136:137], v84, off offset:2816
	global_store_dword v[136:137], v78, off offset:3072
	global_store_dword v[136:137], v76, off offset:3328
	global_store_dword v[136:137], v70, off offset:3584
	global_store_dword v[136:137], v68, off offset:3840
	s_and_saveexec_b64 s[8:9], s[0:1]
	s_cbranch_execz .LBB0_1489
	s_lshl_b64 s[6:7], s[6:7], 2
	s_add_u32 s6, s5, s6
	s_addc_u32 s7, s12, s7
	v_mul_f32_e32 v58, 0x3b800000, v131
	global_store_dword v133, v58, s[6:7]
	s_branch .LBB0_1489

; __device__ __forceinline__ unsigned pk2(float lo, float hi) { return f2bf(lo) | (f2bf(hi) << 16); }
; template <int PART>
; __device__ __forceinline__ void late_weights(const float* const (&in)[34], unsigned char* ws, LAS float* scr, int gw, int NGW, int lane) {
;     ...
;     if (PART < 2) { const int fr = lane & 15, fq = lane >> 4, layer = PART;
;       for (int it = gw; it < 16 * 256; it += NGW) {
;         const int hp = (it >> 8) & 15, d0 = (it & 255) * 16;
;         const float* wq = in[30] + (size_t)layer * D * 2048 + (size_t)(d0 + fr) * 2048 + hp * 128 + fq * 8;
;         const float* sk = in[31] + ((size_t)(layer * 16 + hp) * 128 + fr) * 128 + fq * 8;
;         f32x4 acc[8]; f32x4 ra[2], rb[8][2];
; #pragma unroll
;         for (int kt = 0; kt < 8; ++kt) acc[kt] = (f32x4){0.f, 0.f, 0.f, 0.f};
; #pragma unroll
;         for (int ks = 0; ks < 4; ++ks) {
;             if (ks == 0) { ra[0] = *(const f32x4*)(wq); ra[1] = *(const f32x4*)(wq + 4);
; #pragma unroll
;                 for (int kt = 0; kt < 8; ++kt) { rb[kt][0] = *(const f32x4*)(sk + (size_t)kt * 16 * 128); rb[kt][1] = *(const f32x4*)(sk + (size_t)kt * 16 * 128 + 4); } }
;             u32x4 ao; ao.x = pk2(ra[0][0], ra[0][1]); ao.y = pk2(ra[0][2], ra[0][3]); ao.z = pk2(ra[1][0], ra[1][1]); ao.w = pk2(ra[1][2], ra[1][3]);
;             u32x4 bo[8];
; #pragma unroll
;             for (int kt = 0; kt < 8; ++kt) { bo[kt].x = pk2(rb[kt][0][0], rb[kt][0][1]); bo[kt].y = pk2(rb[kt][0][2], rb[kt][0][3]); bo[kt].z = pk2(rb[kt][1][0], rb[kt][1][1]); bo[kt].w = pk2(rb[kt][1][2], rb[kt][1][3]); }
;             __builtin_amdgcn_sched_barrier(0);
;             if (ks < 3) { ra[0] = *(const f32x4*)(wq + (ks + 1) * 32); ra[1] = *(const f32x4*)(wq + (ks + 1) * 32 + 4);
; #pragma unroll
;                 for (int kt = 0; kt < 8; ++kt) { rb[kt][0] = *(const f32x4*)(sk + (size_t)kt * 16 * 128 + (ks + 1) * 32); rb[kt][1] = *(const f32x4*)(sk + (size_t)kt * 16 * 128 + (ks + 1) * 32 + 4); } }
.LBB0_1498:
	s_and_b32 s85, s5, 0xff0
	v_or_b32_e32 v2, s85, v1
	s_bfe_u32 s86, s4, 0x40008
	v_lshlrev_b32_e32 v54, 13, v2
	v_lshl_add_u64 v[2:3], s[0:1], 0, v[54:55]
	s_lshl_b32 s6, s86, 9
	v_lshl_add_u64 v[2:3], v[2:3], 0, s[6:7]
	v_lshl_add_u64 v[50:51], v[2:3], 0, v[56:57]
	v_lshl_or_b32 v54, s86, 16, v76
	global_load_dwordx4 v[10:13], v[50:51], off
	global_load_dwordx4 v[14:17], v[50:51], off offset:16
	v_lshl_add_u64 v[2:3], s[50:51], 0, v[54:55]
	v_lshl_add_u64 v[60:61], v[2:3], 0, v[56:57]
	v_add_co_u32_e32 v2, vcc, s75, v60
	s_mov_b64 s[22:23], 0x100000
	s_nop 0
	v_addc_co_u32_e32 v3, vcc, 0, v61, vcc
	global_load_dwordx4 v[18:21], v[2:3], off
	v_lshl_add_u64 v[52:53], v[60:61], 0, s[22:23]
	s_mov_b64 s[22:23], 0x10e000
	v_lshl_add_u64 v[2:3], v[60:61], 0, s[22:23]
	global_load_dwordx4 v[2:5], v[2:3], off offset:16
	s_nop 0
	global_load_dwordx4 v[22:25], v[52:53], off offset:16
	v_add_co_u32_e32 v64, vcc, s74, v60
	s_mov_b32 s6, 0x10e000
	s_nop 0
	v_addc_co_u32_e32 v65, vcc, 0, v61, vcc
	v_add_co_u32_e32 v62, vcc, s6, v60
	s_mov_b32 s6, 0x10c000
	s_nop 0
	v_addc_co_u32_e32 v63, vcc, 0, v61, vcc
	v_add_co_u32_e32 v66, vcc, s6, v60
	global_load_dwordx4 v[26:29], v[64:65], off
	s_nop 0
	v_addc_co_u32_e32 v67, vcc, 0, v61, vcc
	v_add_co_u32_e32 v68, vcc, s70, v60
	v_lshl_add_u64 v[6:7], v[60:61], 0, s[14:15]
	s_nop 0
	v_addc_co_u32_e32 v69, vcc, 0, v61, vcc
	v_add_co_u32_e32 v70, vcc, s73, v60
	s_mov_b64 s[22:23], 0x10c000
	s_nop 0
	v_addc_co_u32_e32 v71, vcc, 0, v61, vcc
	global_load_dwordx4 v[34:37], v[70:71], off
	global_load_dwordx4 v[38:41], v[6:7], off offset:16
	v_add_co_u32_e32 v72, vcc, s71, v60
	v_lshl_add_u64 v[30:31], v[60:61], 0, s[22:23]
	s_nop 0
	v_addc_co_u32_e32 v73, vcc, 0, v61, vcc
	s_mov_b64 s[22:23], 0x10a000
	v_lshl_add_u64 v[86:87], v[60:61], 0, s[8:9]
	v_lshl_add_u64 v[94:95], v[60:61], 0, s[10:11]
	v_add_co_u32_e32 v74, vcc, s72, v60
	v_lshl_add_u64 v[102:103], v[60:61], 0, s[12:13]
	v_lshl_add_u64 v[32:33], v[60:61], 0, s[22:23]
	v_addc_co_u32_e32 v75, vcc, 0, v61, vcc
	global_load_dwordx4 v[6:9], v[62:63], off
	global_load_dwordx4 v[42:45], v[30:31], off offset:16
	global_load_dwordx4 v[46:49], v[66:67], off
	global_load_dwordx4 v[78:81], v[32:33], off offset:16
	global_load_dwordx4 v[82:85], v[68:69], off
	s_nop 0
	global_load_dwordx4 v[86:89], v[86:87], off offset:16
	s_nop 0
	global_load_dwordx4 v[90:93], v[72:73], off
	s_nop 0
	global_load_dwordx4 v[94:97], v[94:95], off offset:16
	s_nop 0
	global_load_dwordx4 v[98:101], v[74:75], off
	s_nop 0
	global_load_dwordx4 v[102:105], v[102:103], off offset:16
	s_waitcnt vmcnt(17)
	v_bfe_u32 v30, v10, 16, 1
	v_bfe_u32 v31, v11, 16, 1
	v_add3_u32 v10, v10, v30, s76
	s_waitcnt vmcnt(16)
	v_bfe_u32 v107, v16, 16, 1
	v_add3_u32 v11, v11, v31, s76
	v_lshrrev_b32_e32 v10, 16, v10
	v_add3_u32 v16, v16, v107, s76
	v_and_or_b32 v30, v11, s77, v10
	v_bfe_u32 v10, v17, 16, 1
	v_bfe_u32 v33, v13, 16, 1
	v_lshrrev_b32_e32 v16, 16, v16
	v_add3_u32 v10, v17, v10, s76
	v_add3_u32 v13, v13, v33, s76
	v_and_or_b32 v33, v10, s77, v16
	s_waitcnt vmcnt(15)
	v_bfe_u32 v10, v18, 16, 1
	v_bfe_u32 v32, v12, 16, 1
	v_add3_u32 v10, v18, v10, s76
	v_bfe_u32 v11, v19, 16, 1
	v_add3_u32 v12, v12, v32, s76
	v_lshrrev_b32_e32 v10, 16, v10
	v_add3_u32 v11, v19, v11, s76
	v_lshrrev_b32_e32 v12, 16, v12
	v_and_or_b32 v10, v11, s77, v10
	v_bfe_u32 v11, v20, 16, 1
	v_and_or_b32 v31, v13, s77, v12
	v_add3_u32 v11, v20, v11, s76
	v_bfe_u32 v12, v21, 16, 1
	v_lshrrev_b32_e32 v11, 16, v11
	v_add3_u32 v12, v21, v12, s76
	v_and_or_b32 v11, v12, s77, v11
	s_waitcnt vmcnt(13)
	v_bfe_u32 v12, v22, 16, 1
	v_bfe_u32 v54, v14, 16, 1
	v_add3_u32 v12, v22, v12, s76
	v_bfe_u32 v13, v23, 16, 1
	v_bfe_u32 v106, v15, 16, 1
	v_add3_u32 v14, v14, v54, s76
	v_lshrrev_b32_e32 v12, 16, v12
	v_add3_u32 v13, v23, v13, s76
	v_add3_u32 v15, v15, v106, s76
	v_lshrrev_b32_e32 v14, 16, v14
	v_and_or_b32 v12, v13, s77, v12
	v_bfe_u32 v13, v24, 16, 1
	v_and_or_b32 v32, v15, s77, v14
	v_add3_u32 v13, v24, v13, s76
	v_bfe_u32 v14, v25, 16, 1
	v_lshrrev_b32_e32 v13, 16, v13
	v_add3_u32 v14, v25, v14, s76
	v_and_or_b32 v13, v14, s77, v13
	s_waitcnt vmcnt(12)
	v_bfe_u32 v14, v26, 16, 1
	v_add3_u32 v14, v26, v14, s76
	v_bfe_u32 v15, v27, 16, 1
	v_lshrrev_b32_e32 v14, 16, v14
	v_add3_u32 v15, v27, v15, s76
	v_and_or_b32 v14, v15, s77, v14
	v_bfe_u32 v15, v28, 16, 1
	v_add3_u32 v15, v28, v15, s76
	v_bfe_u32 v16, v29, 16, 1
	v_lshrrev_b32_e32 v15, 16, v15
	v_add3_u32 v16, v29, v16, s76
	v_and_or_b32 v15, v16, s77, v15
	s_waitcnt vmcnt(10)
	v_bfe_u32 v16, v38, 16, 1
	v_add3_u32 v16, v38, v16, s76
	v_bfe_u32 v17, v39, 16, 1
	v_lshrrev_b32_e32 v16, 16, v16
	v_add3_u32 v17, v39, v17, s76
	v_and_or_b32 v16, v17, s77, v16
	v_bfe_u32 v17, v40, 16, 1
	v_add3_u32 v17, v40, v17, s76
	v_bfe_u32 v18, v41, 16, 1
	v_lshrrev_b32_e32 v17, 16, v17
	v_add3_u32 v18, v41, v18, s76
	v_and_or_b32 v17, v18, s77, v17
	v_bfe_u32 v18, v34, 16, 1
	v_add3_u32 v18, v34, v18, s76
	v_bfe_u32 v19, v35, 16, 1
	v_lshrrev_b32_e32 v18, 16, v18
	v_add3_u32 v19, v35, v19, s76
	v_and_or_b32 v18, v19, s77, v18
	v_bfe_u32 v19, v36, 16, 1
	v_add3_u32 v19, v36, v19, s76
	v_bfe_u32 v20, v37, 16, 1
	v_lshrrev_b32_e32 v19, 16, v19
	v_add3_u32 v20, v37, v20, s76
	v_and_or_b32 v19, v20, s77, v19
	s_waitcnt vmcnt(0)
; __device__ __forceinline__ unsigned pk2(float lo, float hi) { return f2bf(lo) | (f2bf(hi) << 16); }
; template <int PART>
; __device__ __forceinline__ void late_weights(const float* const (&in)[34], unsigned char* ws, LAS float* scr, int gw, int NGW, int lane) {
;     ...
;             u32x4 ao; ao.x = pk2(ra[0][0], ra[0][1]); ao.y = pk2(ra[0][2], ra[0][3]); ao.z = pk2(ra[1][0], ra[1][1]); ao.w = pk2(ra[1][2], ra[1][3]);
;             u32x4 bo[8];
; #pragma unroll
;             for (int kt = 0; kt < 8; ++kt) { bo[kt].x = pk2(rb[kt][0][0], rb[kt][0][1]); bo[kt].y = pk2(rb[kt][0][2], rb[kt][0][3]); bo[kt].z = pk2(rb[kt][1][0], rb[kt][1][1]); bo[kt].w = pk2(rb[kt][1][2], rb[kt][1][3]); }
;             __builtin_amdgcn_sched_barrier(0);
;             if (ks < 3) { ra[0] = *(const f32x4*)(wq + (ks + 1) * 32); ra[1] = *(const f32x4*)(wq + (ks + 1) * 32 + 4);
; #pragma unroll
;                 for (int kt = 0; kt < 8; ++kt) { rb[kt][0] = *(const f32x4*)(sk + (size_t)kt * 16 * 128 + (ks + 1) * 32); rb[kt][1] = *(const f32x4*)(sk + (size_t)kt * 16 * 128 + (ks + 1) * 32 + 4); } }
;             __builtin_amdgcn_sched_barrier(0);
; #pragma unroll
;             for (int kt = 0; kt < 8; ++kt) acc[kt] = __builtin_amdgcn_mfma_f32_16x16x32_bf16(__builtin_bit_cast(bf16x8, ao), __builtin_bit_cast(bf16x8, bo[kt]), acc[kt], 0, 0, 0);
	v_bfe_u32 v20, v102, 16, 1
	v_add3_u32 v20, v102, v20, s76
	v_bfe_u32 v21, v103, 16, 1
	v_lshrrev_b32_e32 v20, 16, v20
	v_add3_u32 v21, v103, v21, s76
	v_and_or_b32 v20, v21, s77, v20
	v_bfe_u32 v21, v104, 16, 1
	v_add3_u32 v21, v104, v21, s76
	v_bfe_u32 v22, v105, 16, 1
	v_lshrrev_b32_e32 v21, 16, v21
	v_add3_u32 v22, v105, v22, s76
	v_and_or_b32 v21, v22, s77, v21
	v_bfe_u32 v22, v98, 16, 1
	v_add3_u32 v22, v98, v22, s76
	v_bfe_u32 v23, v99, 16, 1
	v_lshrrev_b32_e32 v22, 16, v22
	v_add3_u32 v23, v99, v23, s76
	v_and_or_b32 v22, v23, s77, v22
	v_bfe_u32 v23, v100, 16, 1
	v_add3_u32 v23, v100, v23, s76
	v_bfe_u32 v24, v101, 16, 1
	v_lshrrev_b32_e32 v23, 16, v23
	v_add3_u32 v24, v101, v24, s76
	v_and_or_b32 v23, v24, s77, v23
	v_bfe_u32 v24, v94, 16, 1
	v_add3_u32 v24, v94, v24, s76
	v_bfe_u32 v25, v95, 16, 1
	v_lshrrev_b32_e32 v24, 16, v24
	v_add3_u32 v25, v95, v25, s76
	v_and_or_b32 v24, v25, s77, v24
	v_bfe_u32 v25, v96, 16, 1
	v_add3_u32 v25, v96, v25, s76
	v_bfe_u32 v26, v97, 16, 1
	v_lshrrev_b32_e32 v25, 16, v25
	v_add3_u32 v26, v97, v26, s76
	v_and_or_b32 v25, v26, s77, v25
	v_bfe_u32 v26, v90, 16, 1
	v_add3_u32 v26, v90, v26, s76
	v_bfe_u32 v27, v91, 16, 1
	v_lshrrev_b32_e32 v26, 16, v26
	v_add3_u32 v27, v91, v27, s76
	v_and_or_b32 v26, v27, s77, v26
	v_bfe_u32 v27, v92, 16, 1
	v_add3_u32 v27, v92, v27, s76
	v_bfe_u32 v28, v93, 16, 1
	v_lshrrev_b32_e32 v27, 16, v27
	v_add3_u32 v28, v93, v28, s76
	v_and_or_b32 v27, v28, s77, v27
	v_bfe_u32 v28, v86, 16, 1
	v_add3_u32 v28, v86, v28, s76
	v_bfe_u32 v29, v87, 16, 1
	v_lshrrev_b32_e32 v28, 16, v28
	v_add3_u32 v29, v87, v29, s76
	v_and_or_b32 v28, v29, s77, v28
	v_bfe_u32 v29, v88, 16, 1
	v_add3_u32 v29, v88, v29, s76
	v_bfe_u32 v34, v89, 16, 1
	v_lshrrev_b32_e32 v29, 16, v29
	v_add3_u32 v34, v89, v34, s76
	v_and_or_b32 v29, v34, s77, v29
	v_bfe_u32 v34, v82, 16, 1
	v_add3_u32 v34, v82, v34, s76
	v_bfe_u32 v35, v83, 16, 1
	v_lshrrev_b32_e32 v34, 16, v34
	v_add3_u32 v35, v83, v35, s76
	v_and_or_b32 v34, v35, s77, v34
	v_bfe_u32 v35, v84, 16, 1
	v_add3_u32 v35, v84, v35, s76
	v_bfe_u32 v36, v85, 16, 1
	v_lshrrev_b32_e32 v35, 16, v35
	v_add3_u32 v36, v85, v36, s76
	v_and_or_b32 v35, v36, s77, v35
	v_bfe_u32 v36, v78, 16, 1
	v_add3_u32 v36, v78, v36, s76
	v_bfe_u32 v37, v79, 16, 1
	v_lshrrev_b32_e32 v36, 16, v36
	v_add3_u32 v37, v79, v37, s76
	v_and_or_b32 v36, v37, s77, v36
	v_bfe_u32 v37, v80, 16, 1
	v_add3_u32 v37, v80, v37, s76
	v_bfe_u32 v38, v81, 16, 1
	v_lshrrev_b32_e32 v37, 16, v37
	v_add3_u32 v38, v81, v38, s76
	v_and_or_b32 v37, v38, s77, v37
	v_bfe_u32 v38, v46, 16, 1
	v_add3_u32 v38, v46, v38, s76
	v_bfe_u32 v39, v47, 16, 1
	v_lshrrev_b32_e32 v38, 16, v38
	v_add3_u32 v39, v47, v39, s76
	v_and_or_b32 v38, v39, s77, v38
	v_bfe_u32 v39, v48, 16, 1
	v_add3_u32 v39, v48, v39, s76
	v_bfe_u32 v40, v49, 16, 1
	v_lshrrev_b32_e32 v39, 16, v39
	v_add3_u32 v40, v49, v40, s76
	v_and_or_b32 v39, v40, s77, v39
	v_bfe_u32 v40, v42, 16, 1
	v_add3_u32 v40, v42, v40, s76
	v_bfe_u32 v41, v43, 16, 1
	v_lshrrev_b32_e32 v40, 16, v40
	v_add3_u32 v41, v43, v41, s76
	v_and_or_b32 v40, v41, s77, v40
	v_bfe_u32 v41, v44, 16, 1
	v_add3_u32 v41, v44, v41, s76
	v_bfe_u32 v42, v45, 16, 1
	v_lshrrev_b32_e32 v41, 16, v41
	v_add3_u32 v42, v45, v42, s76
	v_and_or_b32 v41, v42, s77, v41
	v_bfe_u32 v42, v6, 16, 1
	v_add3_u32 v6, v6, v42, s76
	v_bfe_u32 v42, v7, 16, 1
	v_lshrrev_b32_e32 v6, 16, v6
	v_add3_u32 v7, v7, v42, s76
	v_and_or_b32 v46, v7, s77, v6
	v_bfe_u32 v6, v8, 16, 1
	v_add3_u32 v6, v8, v6, s76
	v_bfe_u32 v7, v9, 16, 1
	v_lshrrev_b32_e32 v6, 16, v6
	v_add3_u32 v7, v9, v7, s76
	v_and_or_b32 v47, v7, s77, v6
	v_bfe_u32 v6, v2, 16, 1
	v_add3_u32 v2, v2, v6, s76
	v_bfe_u32 v6, v3, 16, 1
	v_lshrrev_b32_e32 v2, 16, v2
	v_add3_u32 v3, v3, v6, s76
	v_and_or_b32 v48, v3, s77, v2
	v_bfe_u32 v2, v4, 16, 1
	v_add3_u32 v2, v4, v2, s76
	v_bfe_u32 v3, v5, 16, 1
	v_lshrrev_b32_e32 v2, 16, v2
	v_add3_u32 v3, v5, v3, s76
	v_and_or_b32 v49, v3, s77, v2
	v_lshl_add_u64 v[2:3], v[60:61], 0, s[16:17]
	global_load_dwordx4 v[78:81], v[50:51], off offset:144
	global_load_dwordx4 v[82:85], v[50:51], off offset:128
	global_load_dwordx4 v[86:89], v[52:53], off offset:144
	global_load_dwordx4 v[90:93], v[52:53], off offset:128
	global_load_dwordx4 v[94:97], v[64:65], off offset:128
	global_load_dwordx4 v[98:101], v[2:3], off offset:16
	v_lshl_add_u64 v[2:3], v[60:61], 0, s[18:19]
	v_lshl_add_u64 v[4:5], v[60:61], 0, s[20:21]
	global_load_dwordx4 v[102:105], v[70:71], off offset:128
	global_load_dwordx4 v[106:109], v[74:75], off offset:128
	global_load_dwordx4 v[110:113], v[2:3], off offset:16
	global_load_dwordx4 v[114:117], v[4:5], off offset:16
	v_lshl_add_u64 v[2:3], v[60:61], 0, s[28:29]
	v_lshl_add_u64 v[4:5], v[60:61], 0, s[30:31]
	global_load_dwordx4 v[118:121], v[72:73], off offset:128
	global_load_dwordx4 v[122:125], v[68:69], off offset:128
	global_load_dwordx4 v[126:129], v[2:3], off offset:16
	global_load_dwordx4 v[130:133], v[4:5], off offset:16
	v_lshl_add_u64 v[2:3], v[60:61], 0, s[36:37]
	v_lshl_add_u64 v[4:5], v[60:61], 0, s[38:39]
	global_load_dwordx4 v[134:137], v[66:67], off offset:128
	global_load_dwordx4 v[138:141], v[62:63], off offset:128
	global_load_dwordx4 v[142:145], v[2:3], off offset:16
	global_load_dwordx4 v[42:45], v[4:5], off offset:16
	v_mfma_f32_16x16x32_bf16 v[2:5], v[30:33], v[10:13], 0
	v_mfma_f32_16x16x32_bf16 v[6:9], v[30:33], v[14:17], 0
	v_mfma_f32_16x16x32_bf16 v[10:13], v[30:33], v[18:21], 0
	v_mfma_f32_16x16x32_bf16 v[14:17], v[30:33], v[22:25], 0
	v_mfma_f32_16x16x32_bf16 v[18:21], v[30:33], v[26:29], 0
	v_mfma_f32_16x16x32_bf16 v[22:25], v[30:33], v[34:37], 0
	v_mfma_f32_16x16x32_bf16 v[26:29], v[30:33], v[38:41], 0
	v_mfma_f32_16x16x32_bf16 v[30:33], v[30:33], v[46:49], 0
	s_waitcnt vmcnt(16)
; __device__ __forceinline__ unsigned pk2(float lo, float hi) { return f2bf(lo) | (f2bf(hi) << 16); }
; template <int PART>
; __device__ __forceinline__ void late_weights(const float* const (&in)[34], unsigned char* ws, LAS float* scr, int gw, int NGW, int lane) {
;     ...
;             u32x4 ao; ao.x = pk2(ra[0][0], ra[0][1]); ao.y = pk2(ra[0][2], ra[0][3]); ao.z = pk2(ra[1][0], ra[1][1]); ao.w = pk2(ra[1][2], ra[1][3]);
;             u32x4 bo[8];
; #pragma unroll
;             for (int kt = 0; kt < 8; ++kt) { bo[kt].x = pk2(rb[kt][0][0], rb[kt][0][1]); bo[kt].y = pk2(rb[kt][0][2], rb[kt][0][3]); bo[kt].z = pk2(rb[kt][1][0], rb[kt][1][1]); bo[kt].w = pk2(rb[kt][1][2], rb[kt][1][3]); }
;             __builtin_amdgcn_sched_barrier(0);
;             if (ks < 3) { ra[0] = *(const f32x4*)(wq + (ks + 1) * 32); ra[1] = *(const f32x4*)(wq + (ks + 1) * 32 + 4);
; #pragma unroll
;                 for (int kt = 0; kt < 8; ++kt) { rb[kt][0] = *(const f32x4*)(sk + (size_t)kt * 16 * 128 + (ks + 1) * 32); rb[kt][1] = *(const f32x4*)(sk + (size_t)kt * 16 * 128 + (ks + 1) * 32 + 4); } }
	v_bfe_u32 v34, v82, 16, 1
	v_add3_u32 v34, v82, v34, s76
	v_bfe_u32 v35, v83, 16, 1
	v_lshrrev_b32_e32 v34, 16, v34
	v_add3_u32 v35, v83, v35, s76
	v_and_or_b32 v34, v35, s77, v34
	v_bfe_u32 v35, v84, 16, 1
	v_add3_u32 v35, v84, v35, s76
	v_bfe_u32 v36, v85, 16, 1
	v_lshrrev_b32_e32 v35, 16, v35
	v_add3_u32 v36, v85, v36, s76
	v_and_or_b32 v35, v36, s77, v35
	v_bfe_u32 v36, v78, 16, 1
	v_add3_u32 v36, v78, v36, s76
	v_bfe_u32 v37, v79, 16, 1
	v_lshrrev_b32_e32 v36, 16, v36
	v_add3_u32 v37, v79, v37, s76
	v_and_or_b32 v36, v37, s77, v36
	v_bfe_u32 v37, v80, 16, 1
	v_add3_u32 v37, v80, v37, s76
	v_bfe_u32 v38, v81, 16, 1
	v_lshrrev_b32_e32 v37, 16, v37
	v_add3_u32 v38, v81, v38, s76
	v_and_or_b32 v37, v38, s77, v37
	s_waitcnt vmcnt(14)
	v_bfe_u32 v38, v90, 16, 1
	v_add3_u32 v38, v90, v38, s76
	v_bfe_u32 v39, v91, 16, 1
	v_lshrrev_b32_e32 v38, 16, v38
	v_add3_u32 v39, v91, v39, s76
	v_and_or_b32 v38, v39, s77, v38
	v_bfe_u32 v39, v92, 16, 1
	v_add3_u32 v39, v92, v39, s76
	v_bfe_u32 v40, v93, 16, 1
	v_lshrrev_b32_e32 v39, 16, v39
	v_add3_u32 v40, v93, v40, s76
	v_and_or_b32 v39, v40, s77, v39
	v_bfe_u32 v40, v86, 16, 1
	v_add3_u32 v40, v86, v40, s76
	v_bfe_u32 v41, v87, 16, 1
	v_lshrrev_b32_e32 v40, 16, v40
	v_add3_u32 v41, v87, v41, s76
	v_and_or_b32 v40, v41, s77, v40
	v_bfe_u32 v41, v88, 16, 1
	v_add3_u32 v41, v88, v41, s76
	v_bfe_u32 v46, v89, 16, 1
	v_lshrrev_b32_e32 v41, 16, v41
	v_add3_u32 v46, v89, v46, s76
	v_and_or_b32 v41, v46, s77, v41
	s_waitcnt vmcnt(13)
	v_bfe_u32 v46, v94, 16, 1
	v_add3_u32 v46, v94, v46, s76
	v_bfe_u32 v47, v95, 16, 1
	v_lshrrev_b32_e32 v46, 16, v46
	v_add3_u32 v47, v95, v47, s76
	v_and_or_b32 v46, v47, s77, v46
	v_bfe_u32 v47, v96, 16, 1
	v_add3_u32 v47, v96, v47, s76
	v_bfe_u32 v48, v97, 16, 1
	v_lshrrev_b32_e32 v47, 16, v47
	v_add3_u32 v48, v97, v48, s76
	v_and_or_b32 v47, v48, s77, v47
	s_waitcnt vmcnt(12)
	v_bfe_u32 v48, v98, 16, 1
	v_add3_u32 v48, v98, v48, s76
	v_bfe_u32 v49, v99, 16, 1
	v_lshrrev_b32_e32 v48, 16, v48
	v_add3_u32 v49, v99, v49, s76
	v_and_or_b32 v48, v49, s77, v48
	v_bfe_u32 v49, v100, 16, 1
	v_add3_u32 v49, v100, v49, s76
	v_bfe_u32 v54, v101, 16, 1
	v_lshrrev_b32_e32 v49, 16, v49
	v_add3_u32 v54, v101, v54, s76
	v_and_or_b32 v49, v54, s77, v49
	s_waitcnt vmcnt(11)
	v_bfe_u32 v54, v102, 16, 1
	v_add3_u32 v54, v102, v54, s76
	v_bfe_u32 v78, v103, 16, 1
	v_lshrrev_b32_e32 v54, 16, v54
	v_add3_u32 v78, v103, v78, s76
	v_and_or_b32 v78, v78, s77, v54
	v_bfe_u32 v54, v104, 16, 1
	v_add3_u32 v54, v104, v54, s76
	v_bfe_u32 v79, v105, 16, 1
	v_lshrrev_b32_e32 v54, 16, v54
	v_add3_u32 v79, v105, v79, s76
	v_and_or_b32 v79, v79, s77, v54
	s_waitcnt vmcnt(9)
	v_bfe_u32 v54, v110, 16, 1
	v_add3_u32 v54, v110, v54, s76
	v_bfe_u32 v80, v111, 16, 1
	v_lshrrev_b32_e32 v54, 16, v54
	v_add3_u32 v80, v111, v80, s76
	v_and_or_b32 v80, v80, s77, v54
	v_bfe_u32 v54, v112, 16, 1
	v_add3_u32 v54, v112, v54, s76
	v_bfe_u32 v81, v113, 16, 1
	v_lshrrev_b32_e32 v54, 16, v54
	v_add3_u32 v81, v113, v81, s76
	v_and_or_b32 v81, v81, s77, v54
	v_bfe_u32 v54, v106, 16, 1
	v_add3_u32 v54, v106, v54, s76
	v_bfe_u32 v82, v107, 16, 1
	v_lshrrev_b32_e32 v54, 16, v54
	v_add3_u32 v82, v107, v82, s76
	v_and_or_b32 v82, v82, s77, v54
	v_bfe_u32 v54, v108, 16, 1
	v_add3_u32 v54, v108, v54, s76
	v_bfe_u32 v83, v109, 16, 1
	v_lshrrev_b32_e32 v54, 16, v54
	v_add3_u32 v83, v109, v83, s76
	v_and_or_b32 v83, v83, s77, v54
	s_waitcnt vmcnt(8)
	v_bfe_u32 v54, v114, 16, 1
	v_add3_u32 v54, v114, v54, s76
	v_bfe_u32 v84, v115, 16, 1
	v_lshrrev_b32_e32 v54, 16, v54
	v_add3_u32 v84, v115, v84, s76
	v_and_or_b32 v84, v84, s77, v54
	v_bfe_u32 v54, v116, 16, 1
	v_add3_u32 v54, v116, v54, s76
	v_bfe_u32 v85, v117, 16, 1
	v_lshrrev_b32_e32 v54, 16, v54
	v_add3_u32 v85, v117, v85, s76
	v_and_or_b32 v85, v85, s77, v54
	s_waitcnt vmcnt(7)
	v_bfe_u32 v54, v118, 16, 1
	v_add3_u32 v54, v118, v54, s76
	v_bfe_u32 v86, v119, 16, 1
	v_lshrrev_b32_e32 v54, 16, v54
	v_add3_u32 v86, v119, v86, s76
	v_and_or_b32 v86, v86, s77, v54
	v_bfe_u32 v54, v120, 16, 1
	v_add3_u32 v54, v120, v54, s76
	v_bfe_u32 v87, v121, 16, 1
	v_lshrrev_b32_e32 v54, 16, v54
	v_add3_u32 v87, v121, v87, s76
	v_and_or_b32 v87, v87, s77, v54
	s_waitcnt vmcnt(5)
	v_bfe_u32 v54, v126, 16, 1
	v_add3_u32 v54, v126, v54, s76
	v_bfe_u32 v88, v127, 16, 1
	v_lshrrev_b32_e32 v54, 16, v54
	v_add3_u32 v88, v127, v88, s76
	v_and_or_b32 v88, v88, s77, v54
	v_bfe_u32 v54, v128, 16, 1
	v_add3_u32 v54, v128, v54, s76
	v_bfe_u32 v89, v129, 16, 1
	v_lshrrev_b32_e32 v54, 16, v54
	v_add3_u32 v89, v129, v89, s76
	v_and_or_b32 v89, v89, s77, v54
	v_bfe_u32 v54, v122, 16, 1
	v_add3_u32 v54, v122, v54, s76
	v_bfe_u32 v90, v123, 16, 1
	v_lshrrev_b32_e32 v54, 16, v54
	v_add3_u32 v90, v123, v90, s76
	v_and_or_b32 v90, v90, s77, v54
	v_bfe_u32 v54, v124, 16, 1
	v_add3_u32 v54, v124, v54, s76
	v_bfe_u32 v91, v125, 16, 1
	v_lshrrev_b32_e32 v54, 16, v54
	v_add3_u32 v91, v125, v91, s76
	v_and_or_b32 v91, v91, s77, v54
	s_waitcnt vmcnt(4)
	v_bfe_u32 v54, v130, 16, 1
	v_add3_u32 v54, v130, v54, s76
	v_bfe_u32 v92, v131, 16, 1
	v_lshrrev_b32_e32 v54, 16, v54
	v_add3_u32 v92, v131, v92, s76
	v_and_or_b32 v92, v92, s77, v54
	v_bfe_u32 v54, v132, 16, 1
	v_add3_u32 v54, v132, v54, s76
	v_bfe_u32 v93, v133, 16, 1
	v_lshrrev_b32_e32 v54, 16, v54
	v_add3_u32 v93, v133, v93, s76
	v_and_or_b32 v93, v93, s77, v54
	s_waitcnt vmcnt(3)
	v_bfe_u32 v54, v134, 16, 1
	v_add3_u32 v54, v134, v54, s76
	v_bfe_u32 v94, v135, 16, 1
	v_lshrrev_b32_e32 v54, 16, v54
	v_add3_u32 v94, v135, v94, s76
	v_and_or_b32 v94, v94, s77, v54
	v_bfe_u32 v54, v136, 16, 1
	v_add3_u32 v54, v136, v54, s76
	v_bfe_u32 v95, v137, 16, 1
	v_lshrrev_b32_e32 v54, 16, v54
	v_add3_u32 v95, v137, v95, s76
	v_and_or_b32 v95, v95, s77, v54
	s_waitcnt vmcnt(1)
; __device__ __forceinline__ unsigned pk2(float lo, float hi) { return f2bf(lo) | (f2bf(hi) << 16); }
; template <int PART>
; __device__ __forceinline__ void late_weights(const float* const (&in)[34], unsigned char* ws, LAS float* scr, int gw, int NGW, int lane) {
;     ...
;             u32x4 ao; ao.x = pk2(ra[0][0], ra[0][1]); ao.y = pk2(ra[0][2], ra[0][3]); ao.z = pk2(ra[1][0], ra[1][1]); ao.w = pk2(ra[1][2], ra[1][3]);
;             u32x4 bo[8];
; #pragma unroll
;             for (int kt = 0; kt < 8; ++kt) { bo[kt].x = pk2(rb[kt][0][0], rb[kt][0][1]); bo[kt].y = pk2(rb[kt][0][2], rb[kt][0][3]); bo[kt].z = pk2(rb[kt][1][0], rb[kt][1][1]); bo[kt].w = pk2(rb[kt][1][2], rb[kt][1][3]); }
;             __builtin_amdgcn_sched_barrier(0);
;             if (ks < 3) { ra[0] = *(const f32x4*)(wq + (ks + 1) * 32); ra[1] = *(const f32x4*)(wq + (ks + 1) * 32 + 4);
; #pragma unroll
;                 for (int kt = 0; kt < 8; ++kt) { rb[kt][0] = *(const f32x4*)(sk + (size_t)kt * 16 * 128 + (ks + 1) * 32); rb[kt][1] = *(const f32x4*)(sk + (size_t)kt * 16 * 128 + (ks + 1) * 32 + 4); } }
;             __builtin_amdgcn_sched_barrier(0);
; #pragma unroll
;             for (int kt = 0; kt < 8; ++kt) acc[kt] = __builtin_amdgcn_mfma_f32_16x16x32_bf16(__builtin_bit_cast(bf16x8, ao), __builtin_bit_cast(bf16x8, bo[kt]), acc[kt], 0, 0, 0);
	v_bfe_u32 v54, v142, 16, 1
	v_add3_u32 v54, v142, v54, s76
	v_bfe_u32 v96, v143, 16, 1
	v_lshrrev_b32_e32 v54, 16, v54
	v_add3_u32 v96, v143, v96, s76
	v_and_or_b32 v96, v96, s77, v54
	v_bfe_u32 v54, v144, 16, 1
	v_add3_u32 v54, v144, v54, s76
	v_bfe_u32 v97, v145, 16, 1
	v_lshrrev_b32_e32 v54, 16, v54
	v_add3_u32 v97, v145, v97, s76
	v_and_or_b32 v97, v97, s77, v54
	v_bfe_u32 v54, v138, 16, 1
	v_add3_u32 v54, v138, v54, s76
	v_bfe_u32 v98, v139, 16, 1
	v_lshrrev_b32_e32 v54, 16, v54
	v_add3_u32 v98, v139, v98, s76
	v_and_or_b32 v98, v98, s77, v54
	v_bfe_u32 v54, v140, 16, 1
	v_add3_u32 v54, v140, v54, s76
	v_bfe_u32 v99, v141, 16, 1
	v_lshrrev_b32_e32 v54, 16, v54
	v_add3_u32 v99, v141, v99, s76
	v_and_or_b32 v99, v99, s77, v54
	s_waitcnt vmcnt(0)
	v_bfe_u32 v54, v42, 16, 1
	v_add3_u32 v42, v42, v54, s76
	v_bfe_u32 v54, v43, 16, 1
	v_lshrrev_b32_e32 v42, 16, v42
	v_add3_u32 v43, v43, v54, s76
	v_and_or_b32 v100, v43, s77, v42
	v_bfe_u32 v42, v44, 16, 1
	v_add3_u32 v42, v44, v42, s76
	v_bfe_u32 v43, v45, 16, 1
	v_lshrrev_b32_e32 v42, 16, v42
	v_add3_u32 v43, v45, v43, s76
	v_and_or_b32 v101, v43, s77, v42
	v_lshl_add_u64 v[42:43], v[60:61], 0, s[40:41]
	global_load_dwordx4 v[102:105], v[50:51], off offset:272
	global_load_dwordx4 v[106:109], v[50:51], off offset:256
	global_load_dwordx4 v[110:113], v[52:53], off offset:272
	global_load_dwordx4 v[114:117], v[52:53], off offset:256
	global_load_dwordx4 v[118:121], v[64:65], off offset:256
	global_load_dwordx4 v[122:125], v[42:43], off offset:16
	v_lshl_add_u64 v[42:43], v[60:61], 0, s[42:43]
	v_lshl_add_u64 v[44:45], v[60:61], 0, s[44:45]
	global_load_dwordx4 v[126:129], v[70:71], off offset:256
	global_load_dwordx4 v[130:133], v[74:75], off offset:256
	global_load_dwordx4 v[134:137], v[42:43], off offset:16
	global_load_dwordx4 v[138:141], v[44:45], off offset:16
	v_lshl_add_u64 v[42:43], v[60:61], 0, s[46:47]
	v_lshl_add_u64 v[44:45], v[60:61], 0, s[48:49]
	global_load_dwordx4 v[142:145], v[72:73], off offset:256
	global_load_dwordx4 v[146:149], v[68:69], off offset:256
	global_load_dwordx4 v[150:153], v[42:43], off offset:16
	global_load_dwordx4 v[154:157], v[44:45], off offset:16
	v_lshl_add_u64 v[42:43], v[60:61], 0, s[52:53]
	v_lshl_add_u64 v[44:45], v[60:61], 0, s[54:55]
	global_load_dwordx4 v[158:161], v[66:67], off offset:256
	global_load_dwordx4 v[162:165], v[62:63], off offset:256
	global_load_dwordx4 v[166:169], v[42:43], off offset:16
	s_nop 0
	global_load_dwordx4 v[42:45], v[44:45], off offset:16
	v_mfma_f32_16x16x32_bf16 v[2:5], v[34:37], v[38:41], v[2:5]
	v_mfma_f32_16x16x32_bf16 v[6:9], v[34:37], v[46:49], v[6:9]
	v_mfma_f32_16x16x32_bf16 v[10:13], v[34:37], v[78:81], v[10:13]
	v_mfma_f32_16x16x32_bf16 v[14:17], v[34:37], v[82:85], v[14:17]
	v_mfma_f32_16x16x32_bf16 v[18:21], v[34:37], v[86:89], v[18:21]
	v_mfma_f32_16x16x32_bf16 v[22:25], v[34:37], v[90:93], v[22:25]
	v_mfma_f32_16x16x32_bf16 v[26:29], v[34:37], v[94:97], v[26:29]
	v_mfma_f32_16x16x32_bf16 v[30:33], v[34:37], v[98:101], v[30:33]
	s_waitcnt vmcnt(16)
	v_bfe_u32 v34, v106, 16, 1
	v_add3_u32 v34, v106, v34, s76
	v_bfe_u32 v35, v107, 16, 1
	v_lshrrev_b32_e32 v34, 16, v34
	v_add3_u32 v35, v107, v35, s76
	v_and_or_b32 v34, v35, s77, v34
	v_bfe_u32 v35, v108, 16, 1
	v_add3_u32 v35, v108, v35, s76
	v_bfe_u32 v36, v109, 16, 1
	v_lshrrev_b32_e32 v35, 16, v35
	v_add3_u32 v36, v109, v36, s76
	v_and_or_b32 v35, v36, s77, v35
	v_bfe_u32 v36, v102, 16, 1
	v_add3_u32 v36, v102, v36, s76
	v_bfe_u32 v37, v103, 16, 1
	v_lshrrev_b32_e32 v36, 16, v36
	v_add3_u32 v37, v103, v37, s76
	v_and_or_b32 v36, v37, s77, v36
	v_bfe_u32 v37, v104, 16, 1
	v_add3_u32 v37, v104, v37, s76
	v_bfe_u32 v38, v105, 16, 1
	v_lshrrev_b32_e32 v37, 16, v37
	v_add3_u32 v38, v105, v38, s76
	v_and_or_b32 v37, v38, s77, v37
	s_waitcnt vmcnt(14)
	v_bfe_u32 v38, v114, 16, 1
	v_add3_u32 v38, v114, v38, s76
	v_bfe_u32 v39, v115, 16, 1
	v_lshrrev_b32_e32 v38, 16, v38
	v_add3_u32 v39, v115, v39, s76
	v_and_or_b32 v46, v39, s77, v38
	v_bfe_u32 v38, v116, 16, 1
	v_add3_u32 v38, v116, v38, s76
	v_bfe_u32 v39, v117, 16, 1
	v_lshrrev_b32_e32 v38, 16, v38
	v_add3_u32 v39, v117, v39, s76
	v_and_or_b32 v47, v39, s77, v38
	v_bfe_u32 v38, v110, 16, 1
	v_add3_u32 v38, v110, v38, s76
	v_bfe_u32 v39, v111, 16, 1
	v_lshrrev_b32_e32 v38, 16, v38
	v_add3_u32 v39, v111, v39, s76
	v_and_or_b32 v48, v39, s77, v38
	v_bfe_u32 v38, v112, 16, 1
	v_add3_u32 v38, v112, v38, s76
	v_bfe_u32 v39, v113, 16, 1
	v_lshrrev_b32_e32 v38, 16, v38
	v_add3_u32 v39, v113, v39, s76
	v_and_or_b32 v49, v39, s77, v38
	s_waitcnt vmcnt(13)
	v_bfe_u32 v38, v118, 16, 1
	v_add3_u32 v38, v118, v38, s76
	v_bfe_u32 v39, v119, 16, 1
	v_lshrrev_b32_e32 v38, 16, v38
	v_add3_u32 v39, v119, v39, s76
	v_and_or_b32 v78, v39, s77, v38
	v_bfe_u32 v38, v120, 16, 1
	v_add3_u32 v38, v120, v38, s76
	v_bfe_u32 v39, v121, 16, 1
	v_lshrrev_b32_e32 v38, 16, v38
	v_add3_u32 v39, v121, v39, s76
	v_and_or_b32 v79, v39, s77, v38
	s_waitcnt vmcnt(12)
	v_bfe_u32 v38, v122, 16, 1
	v_add3_u32 v38, v122, v38, s76
	v_bfe_u32 v39, v123, 16, 1
	v_lshrrev_b32_e32 v38, 16, v38
	v_add3_u32 v39, v123, v39, s76
	v_and_or_b32 v80, v39, s77, v38
	v_bfe_u32 v38, v124, 16, 1
	v_add3_u32 v38, v124, v38, s76
	v_bfe_u32 v39, v125, 16, 1
	v_lshrrev_b32_e32 v38, 16, v38
	v_add3_u32 v39, v125, v39, s76
	v_and_or_b32 v81, v39, s77, v38
	s_waitcnt vmcnt(11)
	v_bfe_u32 v38, v126, 16, 1
	v_add3_u32 v38, v126, v38, s76
	v_bfe_u32 v39, v127, 16, 1
	v_lshrrev_b32_e32 v38, 16, v38
	v_add3_u32 v39, v127, v39, s76
	v_and_or_b32 v82, v39, s77, v38
	v_bfe_u32 v38, v128, 16, 1
	v_add3_u32 v38, v128, v38, s76
	v_bfe_u32 v39, v129, 16, 1
	v_lshrrev_b32_e32 v38, 16, v38
	v_add3_u32 v39, v129, v39, s76
	v_and_or_b32 v83, v39, s77, v38
	s_waitcnt vmcnt(9)
; __device__ __forceinline__ unsigned pk2(float lo, float hi) { return f2bf(lo) | (f2bf(hi) << 16); }
; template <int PART>
; __device__ __forceinline__ void late_weights(const float* const (&in)[34], unsigned char* ws, LAS float* scr, int gw, int NGW, int lane) {
;     ...
;             u32x4 ao; ao.x = pk2(ra[0][0], ra[0][1]); ao.y = pk2(ra[0][2], ra[0][3]); ao.z = pk2(ra[1][0], ra[1][1]); ao.w = pk2(ra[1][2], ra[1][3]);
;             u32x4 bo[8];
; #pragma unroll
;             for (int kt = 0; kt < 8; ++kt) { bo[kt].x = pk2(rb[kt][0][0], rb[kt][0][1]); bo[kt].y = pk2(rb[kt][0][2], rb[kt][0][3]); bo[kt].z = pk2(rb[kt][1][0], rb[kt][1][1]); bo[kt].w = pk2(rb[kt][1][2], rb[kt][1][3]); }
;             __builtin_amdgcn_sched_barrier(0);
;             if (ks < 3) { ra[0] = *(const f32x4*)(wq + (ks + 1) * 32); ra[1] = *(const f32x4*)(wq + (ks + 1) * 32 + 4);
; #pragma unroll
;                 for (int kt = 0; kt < 8; ++kt) { rb[kt][0] = *(const f32x4*)(sk + (size_t)kt * 16 * 128 + (ks + 1) * 32); rb[kt][1] = *(const f32x4*)(sk + (size_t)kt * 16 * 128 + (ks + 1) * 32 + 4); } }
;             __builtin_amdgcn_sched_barrier(0);
; #pragma unroll
;             for (int kt = 0; kt < 8; ++kt) acc[kt] = __builtin_amdgcn_mfma_f32_16x16x32_bf16(__builtin_bit_cast(bf16x8, ao), __builtin_bit_cast(bf16x8, bo[kt]), acc[kt], 0, 0, 0);
	v_bfe_u32 v38, v134, 16, 1
	v_add3_u32 v38, v134, v38, s76
	v_bfe_u32 v39, v135, 16, 1
	v_lshrrev_b32_e32 v38, 16, v38
	v_add3_u32 v39, v135, v39, s76
	v_and_or_b32 v84, v39, s77, v38
	v_bfe_u32 v38, v136, 16, 1
	v_add3_u32 v38, v136, v38, s76
	v_bfe_u32 v39, v137, 16, 1
	v_lshrrev_b32_e32 v38, 16, v38
	v_add3_u32 v39, v137, v39, s76
	v_and_or_b32 v85, v39, s77, v38
	v_bfe_u32 v38, v130, 16, 1
	v_add3_u32 v38, v130, v38, s76
	v_bfe_u32 v39, v131, 16, 1
	v_lshrrev_b32_e32 v38, 16, v38
	v_add3_u32 v39, v131, v39, s76
	v_and_or_b32 v86, v39, s77, v38
	v_bfe_u32 v38, v132, 16, 1
	v_add3_u32 v38, v132, v38, s76
	v_bfe_u32 v39, v133, 16, 1
	v_lshrrev_b32_e32 v38, 16, v38
	v_add3_u32 v39, v133, v39, s76
	v_and_or_b32 v87, v39, s77, v38
	s_waitcnt vmcnt(8)
	v_bfe_u32 v38, v138, 16, 1
	v_add3_u32 v38, v138, v38, s76
	v_bfe_u32 v39, v139, 16, 1
	v_lshrrev_b32_e32 v38, 16, v38
	v_add3_u32 v39, v139, v39, s76
	v_and_or_b32 v88, v39, s77, v38
	v_bfe_u32 v38, v140, 16, 1
	v_add3_u32 v38, v140, v38, s76
	v_bfe_u32 v39, v141, 16, 1
	v_lshrrev_b32_e32 v38, 16, v38
	v_add3_u32 v39, v141, v39, s76
	v_and_or_b32 v89, v39, s77, v38
	s_waitcnt vmcnt(7)
	v_bfe_u32 v38, v142, 16, 1
	v_add3_u32 v38, v142, v38, s76
	v_bfe_u32 v39, v143, 16, 1
	v_lshrrev_b32_e32 v38, 16, v38
	v_add3_u32 v39, v143, v39, s76
	v_and_or_b32 v90, v39, s77, v38
	v_bfe_u32 v38, v144, 16, 1
	v_add3_u32 v38, v144, v38, s76
	v_bfe_u32 v39, v145, 16, 1
	v_lshrrev_b32_e32 v38, 16, v38
	v_add3_u32 v39, v145, v39, s76
	v_and_or_b32 v91, v39, s77, v38
	s_waitcnt vmcnt(5)
	v_bfe_u32 v38, v150, 16, 1
	v_add3_u32 v38, v150, v38, s76
	v_bfe_u32 v39, v151, 16, 1
	v_lshrrev_b32_e32 v38, 16, v38
	v_add3_u32 v39, v151, v39, s76
	v_and_or_b32 v92, v39, s77, v38
	v_bfe_u32 v38, v152, 16, 1
	v_add3_u32 v38, v152, v38, s76
	v_bfe_u32 v39, v153, 16, 1
	v_lshrrev_b32_e32 v38, 16, v38
	v_add3_u32 v39, v153, v39, s76
	v_and_or_b32 v93, v39, s77, v38
	v_bfe_u32 v38, v146, 16, 1
	v_add3_u32 v38, v146, v38, s76
	v_bfe_u32 v39, v147, 16, 1
	v_lshrrev_b32_e32 v38, 16, v38
	v_add3_u32 v39, v147, v39, s76
	v_and_or_b32 v94, v39, s77, v38
	v_bfe_u32 v38, v148, 16, 1
	v_add3_u32 v38, v148, v38, s76
	v_bfe_u32 v39, v149, 16, 1
	v_lshrrev_b32_e32 v38, 16, v38
	v_add3_u32 v39, v149, v39, s76
	v_and_or_b32 v95, v39, s77, v38
	s_waitcnt vmcnt(4)
	v_bfe_u32 v38, v154, 16, 1
	v_add3_u32 v38, v154, v38, s76
	v_bfe_u32 v39, v155, 16, 1
	v_lshrrev_b32_e32 v38, 16, v38
	v_add3_u32 v39, v155, v39, s76
	v_and_or_b32 v96, v39, s77, v38
	v_bfe_u32 v38, v156, 16, 1
	v_add3_u32 v38, v156, v38, s76
	v_bfe_u32 v39, v157, 16, 1
	v_lshrrev_b32_e32 v38, 16, v38
	v_add3_u32 v39, v157, v39, s76
	v_and_or_b32 v97, v39, s77, v38
	s_waitcnt vmcnt(3)
	v_bfe_u32 v38, v158, 16, 1
	v_add3_u32 v38, v158, v38, s76
	v_bfe_u32 v39, v159, 16, 1
	v_lshrrev_b32_e32 v38, 16, v38
	v_add3_u32 v39, v159, v39, s76
	v_and_or_b32 v98, v39, s77, v38
	v_bfe_u32 v38, v160, 16, 1
	v_add3_u32 v38, v160, v38, s76
	v_bfe_u32 v39, v161, 16, 1
	v_lshrrev_b32_e32 v38, 16, v38
	v_add3_u32 v39, v161, v39, s76
	v_and_or_b32 v99, v39, s77, v38
	s_waitcnt vmcnt(1)
	v_bfe_u32 v38, v166, 16, 1
	v_add3_u32 v38, v166, v38, s76
	v_bfe_u32 v39, v167, 16, 1
	v_lshrrev_b32_e32 v38, 16, v38
	v_add3_u32 v39, v167, v39, s76
	v_and_or_b32 v100, v39, s77, v38
	v_bfe_u32 v38, v168, 16, 1
	v_add3_u32 v38, v168, v38, s76
	v_bfe_u32 v39, v169, 16, 1
	v_lshrrev_b32_e32 v38, 16, v38
	v_add3_u32 v39, v169, v39, s76
	v_and_or_b32 v101, v39, s77, v38
	v_bfe_u32 v38, v162, 16, 1
	v_add3_u32 v38, v162, v38, s76
	v_bfe_u32 v39, v163, 16, 1
	v_lshrrev_b32_e32 v38, 16, v38
	v_add3_u32 v39, v163, v39, s76
	v_and_or_b32 v102, v39, s77, v38
	v_bfe_u32 v38, v164, 16, 1
	v_add3_u32 v38, v164, v38, s76
	v_bfe_u32 v39, v165, 16, 1
	v_lshrrev_b32_e32 v38, 16, v38
	v_add3_u32 v39, v165, v39, s76
	v_and_or_b32 v103, v39, s77, v38
	s_waitcnt vmcnt(0)
	v_bfe_u32 v38, v42, 16, 1
	v_add3_u32 v38, v42, v38, s76
	v_bfe_u32 v39, v43, 16, 1
	v_lshrrev_b32_e32 v38, 16, v38
	v_add3_u32 v39, v43, v39, s76
	v_and_or_b32 v104, v39, s77, v38
	v_bfe_u32 v38, v44, 16, 1
	v_add3_u32 v38, v44, v38, s76
	v_bfe_u32 v39, v45, 16, 1
	v_lshrrev_b32_e32 v38, 16, v38
	v_add3_u32 v39, v45, v39, s76
	v_and_or_b32 v105, v39, s77, v38
	global_load_dwordx4 v[106:109], v[50:51], off offset:400
	global_load_dwordx4 v[110:113], v[50:51], off offset:384
	global_load_dwordx4 v[38:41], v[52:53], off offset:400
	global_load_dwordx4 v[42:45], v[52:53], off offset:384
	v_lshl_add_u64 v[50:51], v[60:61], 0, s[56:57]
	global_load_dwordx4 v[114:117], v[64:65], off offset:384
	s_nop 0
	global_load_dwordx4 v[50:53], v[50:51], off offset:16
	v_lshl_add_u64 v[64:65], v[60:61], 0, s[58:59]
	v_lshl_add_u64 v[130:131], v[60:61], 0, s[60:61]
	global_load_dwordx4 v[118:121], v[70:71], off offset:384
	global_load_dwordx4 v[122:125], v[74:75], off offset:384
	global_load_dwordx4 v[126:129], v[64:65], off offset:16
	s_nop 0
	global_load_dwordx4 v[130:133], v[130:131], off offset:16
	v_lshl_add_u64 v[64:65], v[60:61], 0, s[62:63]
	v_lshl_add_u64 v[74:75], v[60:61], 0, s[64:65]
	global_load_dwordx4 v[70:73], v[72:73], off offset:384
	s_nop 0
	global_load_dwordx4 v[134:137], v[68:69], off offset:384
	global_load_dwordx4 v[138:141], v[64:65], off offset:16
	global_load_dwordx4 v[142:145], v[74:75], off offset:16
	v_lshl_add_u64 v[68:69], v[60:61], 0, s[66:67]
	v_lshl_add_u64 v[74:75], v[60:61], 0, s[68:69]
	global_load_dwordx4 v[64:67], v[66:67], off offset:384
	s_nop 0
	global_load_dwordx4 v[60:63], v[62:63], off offset:384
	s_nop 0
	global_load_dwordx4 v[146:149], v[68:69], off offset:16
	global_load_dwordx4 v[150:153], v[74:75], off offset:16
	v_mfma_f32_16x16x32_bf16 v[2:5], v[34:37], v[46:49], v[2:5]
	v_mfma_f32_16x16x32_bf16 v[6:9], v[34:37], v[78:81], v[6:9]
	v_mfma_f32_16x16x32_bf16 v[10:13], v[34:37], v[82:85], v[10:13]
	v_mfma_f32_16x16x32_bf16 v[14:17], v[34:37], v[86:89], v[14:17]
	v_mfma_f32_16x16x32_bf16 v[18:21], v[34:37], v[90:93], v[18:21]
	v_mfma_f32_16x16x32_bf16 v[22:25], v[34:37], v[94:97], v[22:25]
	v_mfma_f32_16x16x32_bf16 v[26:29], v[34:37], v[98:101], v[26:29]
	v_mfma_f32_16x16x32_bf16 v[30:33], v[34:37], v[102:105], v[30:33]
	s_waitcnt vmcnt(16)
; __device__ __forceinline__ unsigned pk2(float lo, float hi) { return f2bf(lo) | (f2bf(hi) << 16); }
; template <int PART>
; __device__ __forceinline__ void late_weights(const float* const (&in)[34], unsigned char* ws, LAS float* scr, int gw, int NGW, int lane) {
;     ...
;             u32x4 ao; ao.x = pk2(ra[0][0], ra[0][1]); ao.y = pk2(ra[0][2], ra[0][3]); ao.z = pk2(ra[1][0], ra[1][1]); ao.w = pk2(ra[1][2], ra[1][3]);
;             u32x4 bo[8];
; #pragma unroll
;             for (int kt = 0; kt < 8; ++kt) { bo[kt].x = pk2(rb[kt][0][0], rb[kt][0][1]); bo[kt].y = pk2(rb[kt][0][2], rb[kt][0][3]); bo[kt].z = pk2(rb[kt][1][0], rb[kt][1][1]); bo[kt].w = pk2(rb[kt][1][2], rb[kt][1][3]); }
;             __builtin_amdgcn_sched_barrier(0);
;             if (ks < 3) { ra[0] = *(const f32x4*)(wq + (ks + 1) * 32); ra[1] = *(const f32x4*)(wq + (ks + 1) * 32 + 4);
; #pragma unroll
;                 for (int kt = 0; kt < 8; ++kt) { rb[kt][0] = *(const f32x4*)(sk + (size_t)kt * 16 * 128 + (ks + 1) * 32); rb[kt][1] = *(const f32x4*)(sk + (size_t)kt * 16 * 128 + (ks + 1) * 32 + 4); } }
	v_bfe_u32 v35, v110, 16, 1
	v_bfe_u32 v34, v111, 16, 1
	v_add3_u32 v35, v110, v35, s76
	v_add3_u32 v34, v111, v34, s76
	v_lshrrev_b32_e32 v35, 16, v35
	v_bfe_u32 v36, v112, 16, 1
	v_and_or_b32 v34, v34, s77, v35
	v_bfe_u32 v35, v113, 16, 1
	v_add3_u32 v36, v112, v36, s76
	v_add3_u32 v35, v113, v35, s76
	v_lshrrev_b32_e32 v36, 16, v36
	v_bfe_u32 v37, v106, 16, 1
	v_and_or_b32 v35, v35, s77, v36
	v_bfe_u32 v36, v107, 16, 1
	v_add3_u32 v37, v106, v37, s76
	v_add3_u32 v36, v107, v36, s76
	v_lshrrev_b32_e32 v37, 16, v37
	v_bfe_u32 v46, v108, 16, 1
	v_and_or_b32 v36, v36, s77, v37
	v_bfe_u32 v37, v109, 16, 1
	v_add3_u32 v46, v108, v46, s76
	v_add3_u32 v37, v109, v37, s76
	v_lshrrev_b32_e32 v46, 16, v46
	s_waitcnt vmcnt(2)
	v_bfe_u32 v47, v60, 16, 1
	v_and_or_b32 v37, v37, s77, v46
	v_bfe_u32 v46, v61, 16, 1
	v_add3_u32 v47, v60, v47, s76
	v_add3_u32 v46, v61, v46, s76
	v_lshrrev_b32_e32 v47, 16, v47
	v_bfe_u32 v48, v62, 16, 1
	v_and_or_b32 v46, v46, s77, v47
	v_bfe_u32 v47, v63, 16, 1
	v_add3_u32 v48, v62, v48, s76
	v_add3_u32 v47, v63, v47, s76
	v_lshrrev_b32_e32 v48, 16, v48
	s_waitcnt vmcnt(0)
	v_bfe_u32 v49, v150, 16, 1
	v_and_or_b32 v47, v47, s77, v48
	v_bfe_u32 v48, v151, 16, 1
	v_add3_u32 v49, v150, v49, s76
	v_add3_u32 v48, v151, v48, s76
	v_lshrrev_b32_e32 v49, 16, v49
	v_bfe_u32 v54, v152, 16, 1
	v_and_or_b32 v48, v48, s77, v49
	v_bfe_u32 v49, v153, 16, 1
	v_add3_u32 v54, v152, v54, s76
	v_add3_u32 v49, v153, v49, s76
	v_lshrrev_b32_e32 v54, 16, v54
	v_bfe_u32 v60, v64, 16, 1
	v_and_or_b32 v49, v49, s77, v54
	v_bfe_u32 v54, v65, 16, 1
	v_add3_u32 v60, v64, v60, s76
	v_add3_u32 v54, v65, v54, s76
	v_lshrrev_b32_e32 v60, 16, v60
	v_bfe_u32 v61, v66, 16, 1
	v_and_or_b32 v60, v54, s77, v60
	v_bfe_u32 v54, v67, 16, 1
	v_add3_u32 v61, v66, v61, s76
	v_add3_u32 v54, v67, v54, s76
	v_lshrrev_b32_e32 v61, 16, v61
	v_bfe_u32 v62, v146, 16, 1
	v_and_or_b32 v61, v54, s77, v61
	v_bfe_u32 v54, v147, 16, 1
	v_add3_u32 v62, v146, v62, s76
	v_add3_u32 v54, v147, v54, s76
	v_lshrrev_b32_e32 v62, 16, v62
	v_bfe_u32 v63, v148, 16, 1
	v_and_or_b32 v62, v54, s77, v62
	v_bfe_u32 v54, v149, 16, 1
	v_add3_u32 v63, v148, v63, s76
	v_add3_u32 v54, v149, v54, s76
	v_lshrrev_b32_e32 v63, 16, v63
	v_bfe_u32 v64, v134, 16, 1
	v_and_or_b32 v63, v54, s77, v63
	v_bfe_u32 v54, v135, 16, 1
	v_add3_u32 v64, v134, v64, s76
	v_add3_u32 v54, v135, v54, s76
	v_lshrrev_b32_e32 v64, 16, v64
	v_bfe_u32 v65, v136, 16, 1
	v_and_or_b32 v64, v54, s77, v64
	v_bfe_u32 v54, v137, 16, 1
	v_add3_u32 v65, v136, v65, s76
	v_add3_u32 v54, v137, v54, s76
	v_lshrrev_b32_e32 v65, 16, v65
	v_bfe_u32 v66, v142, 16, 1
	v_and_or_b32 v65, v54, s77, v65
	v_bfe_u32 v54, v143, 16, 1
	v_add3_u32 v66, v142, v66, s76
	v_add3_u32 v54, v143, v54, s76
	v_lshrrev_b32_e32 v66, 16, v66
	v_bfe_u32 v67, v144, 16, 1
	v_and_or_b32 v66, v54, s77, v66
	v_bfe_u32 v54, v145, 16, 1
	v_add3_u32 v67, v144, v67, s76
	v_add3_u32 v54, v145, v54, s76
	v_lshrrev_b32_e32 v67, 16, v67
	v_bfe_u32 v68, v70, 16, 1
	v_and_or_b32 v67, v54, s77, v67
	v_bfe_u32 v54, v71, 16, 1
	v_add3_u32 v68, v70, v68, s76
	v_add3_u32 v54, v71, v54, s76
	v_lshrrev_b32_e32 v68, 16, v68
	v_bfe_u32 v69, v72, 16, 1
	v_and_or_b32 v68, v54, s77, v68
	v_bfe_u32 v54, v73, 16, 1
	v_add3_u32 v69, v72, v69, s76
	v_add3_u32 v54, v73, v54, s76
	v_lshrrev_b32_e32 v69, 16, v69
	v_bfe_u32 v70, v138, 16, 1
	v_and_or_b32 v69, v54, s77, v69
	v_bfe_u32 v54, v139, 16, 1
	v_add3_u32 v70, v138, v70, s76
	v_add3_u32 v54, v139, v54, s76
	v_lshrrev_b32_e32 v70, 16, v70
	v_bfe_u32 v71, v140, 16, 1
	v_and_or_b32 v70, v54, s77, v70
	v_bfe_u32 v54, v141, 16, 1
	v_add3_u32 v71, v140, v71, s76
	v_add3_u32 v54, v141, v54, s76
	v_lshrrev_b32_e32 v71, 16, v71
	v_bfe_u32 v72, v122, 16, 1
	v_and_or_b32 v71, v54, s77, v71
	v_bfe_u32 v54, v123, 16, 1
	v_add3_u32 v72, v122, v72, s76
	v_add3_u32 v54, v123, v54, s76
	v_lshrrev_b32_e32 v72, 16, v72
	v_bfe_u32 v73, v124, 16, 1
	v_and_or_b32 v72, v54, s77, v72
	v_bfe_u32 v54, v125, 16, 1
	v_add3_u32 v73, v124, v73, s76
	v_add3_u32 v54, v125, v54, s76
	v_lshrrev_b32_e32 v73, 16, v73
	v_bfe_u32 v74, v130, 16, 1
	v_and_or_b32 v73, v54, s77, v73
	v_bfe_u32 v54, v131, 16, 1
	v_add3_u32 v74, v130, v74, s76
	v_add3_u32 v54, v131, v54, s76
	v_lshrrev_b32_e32 v74, 16, v74
	v_bfe_u32 v75, v132, 16, 1
	v_and_or_b32 v74, v54, s77, v74
	v_bfe_u32 v54, v133, 16, 1
	v_add3_u32 v75, v132, v75, s76
	v_add3_u32 v54, v133, v54, s76
	v_lshrrev_b32_e32 v75, 16, v75
	v_bfe_u32 v78, v118, 16, 1
	v_and_or_b32 v75, v54, s77, v75
	v_bfe_u32 v54, v119, 16, 1
	v_add3_u32 v78, v118, v78, s76
	v_add3_u32 v54, v119, v54, s76
	v_lshrrev_b32_e32 v78, 16, v78
	v_bfe_u32 v79, v120, 16, 1
	v_and_or_b32 v78, v54, s77, v78
	v_bfe_u32 v54, v121, 16, 1
	v_add3_u32 v79, v120, v79, s76
	v_add3_u32 v54, v121, v54, s76
	v_lshrrev_b32_e32 v79, 16, v79
	v_bfe_u32 v80, v126, 16, 1
	v_and_or_b32 v79, v54, s77, v79
	v_bfe_u32 v54, v127, 16, 1
	v_add3_u32 v80, v126, v80, s76
	v_add3_u32 v54, v127, v54, s76
	v_lshrrev_b32_e32 v80, 16, v80
	v_bfe_u32 v81, v128, 16, 1
	v_and_or_b32 v80, v54, s77, v80
	v_bfe_u32 v54, v129, 16, 1
	v_add3_u32 v81, v128, v81, s76
	v_add3_u32 v54, v129, v54, s76
	v_lshrrev_b32_e32 v81, 16, v81
	v_bfe_u32 v82, v114, 16, 1
	v_and_or_b32 v81, v54, s77, v81
	v_bfe_u32 v54, v115, 16, 1
	v_add3_u32 v82, v114, v82, s76
	v_add3_u32 v54, v115, v54, s76
	v_lshrrev_b32_e32 v82, 16, v82
	v_bfe_u32 v83, v116, 16, 1
	v_and_or_b32 v82, v54, s77, v82
	v_bfe_u32 v54, v117, 16, 1
	v_add3_u32 v83, v116, v83, s76
	v_add3_u32 v54, v117, v54, s76
	v_lshrrev_b32_e32 v83, 16, v83
	v_and_or_b32 v83, v54, s77, v83
	v_bfe_u32 v54, v51, 16, 1
	v_add3_u32 v51, v51, v54, s76
	v_bfe_u32 v54, v50, 16, 1
; __device__ __forceinline__ void peer_row_load(f32x4 (&v)[16], const float* const (&in)[34], int it, int layer, int lane) {
;     const int tbl = it >= NEXP, r = it - tbl * NEXP + layer * NEXP;
;     const f32x4* src = (const f32x4*)((tbl ? in[33] : in[32]) + (size_t)r * D) + lane;
; #pragma unroll
;     for (int j = 0; j < 16; ++j) v[j] = src[64 * j];
; }
; __device__ __forceinline__ void peer_row_store(const f32x4 (&v)[16], unsigned char* ws, int it, int layer, int lane) {
;     const int tbl = it >= NEXP, r = it - tbl * NEXP + layer * NEXP;
;     float am = 0.f;
; #pragma unroll
;     for (int j = 0; j < 16; ++j) am = fmaxf(fmaxf(am, fmaxf(fabsf(v[j][0]), fabsf(v[j][1]))), fmaxf(fabsf(v[j][2]), fabsf(v[j][3])));
;     am = __uint_as_float(max64u(__float_as_uint(am)));
;     const float q = am > 0.f ? 256.0f / am : 0.f;
;     unsigned* dst = (unsigned*)(ws + (tbl ? WS_PV : WS_PU) + (size_t)r * D) + lane;
;     if (tbl) {
;         const int rl = it - NEXP;
;         unsigned char* pvl = ws + WS_PV + (size_t)layer * NEXP * D + (size_t)rl * 8 + (lane & 1) * 4;
;         unsigned char* pvg = ws + WS_PV + (size_t)layer * NEXP * D + (size_t)NEXP * 2048 + (size_t)rl * 2048 + 4 * lane;
; #pragma unroll
;         for (int j = 0; j < 16; ++j) { int w = __builtin_amdgcn_cvt_pk_bf8_f32(v[j][0] * q, v[j][1] * q, 0, false); w = __builtin_amdgcn_cvt_pk_bf8_f32(v[j][2] * q, v[j][3] * q, w, true);
;             if (j < 8) *(unsigned*)(pvl + (size_t)((lane >> 1) + 32 * j) * (NEXP * 8)) = (unsigned)w;
;             else *(unsigned*)(pvg + 256 * (j - 8)) = (unsigned)w; }
;     } else {
; #pragma unroll
; template <int PART>
; __device__ __forceinline__ void late_weights(const float* const (&in)[34], unsigned char* ws, LAS float* scr, int gw, int NGW, int lane) {
;     ...
;             for (int kt = 0; kt < 8; ++kt) acc[kt] = __builtin_amdgcn_mfma_f32_16x16x32_bf16(__builtin_bit_cast(bf16x8, ao), __builtin_bit_cast(bf16x8, bo[kt]), acc[kt], 0, 0, 0);
;             __builtin_amdgcn_sched_barrier(0);
;         }
; #pragma unroll
;         for (int kt = 0; kt < 8; ++kt) { const f32x4 v = acc[kt]; u32x2 o; o.x = cvt_pk_bf16(v[0], v[1]); o.y = cvt_pk_bf16(v[2], v[3]);
;             *(u32x2*)(WST + ((size_t)layer * 2048 + hp * 128 + kt * 16 + fr) * D + d0 + 4 * fq) = o; }
;       } }
	v_add3_u32 v50, v50, v54, s76
	v_lshrrev_b32_e32 v50, 16, v50
	v_and_or_b32 v84, v51, s77, v50
	v_bfe_u32 v51, v52, 16, 1
	v_bfe_u32 v50, v53, 16, 1
	v_add3_u32 v51, v52, v51, s76
	v_add3_u32 v50, v53, v50, s76
	v_lshrrev_b32_e32 v51, 16, v51
	v_and_or_b32 v85, v50, s77, v51
	v_bfe_u32 v50, v43, 16, 1
	v_add3_u32 v43, v43, v50, s76
	v_bfe_u32 v50, v42, 16, 1
	v_add3_u32 v42, v42, v50, s76
	v_lshrrev_b32_e32 v42, 16, v42
	v_and_or_b32 v42, v43, s77, v42
	v_bfe_u32 v43, v45, 16, 1
	v_add3_u32 v43, v45, v43, s76
	v_bfe_u32 v45, v44, 16, 1
	v_add3_u32 v44, v44, v45, s76
	v_lshrrev_b32_e32 v44, 16, v44
	v_and_or_b32 v43, v43, s77, v44
	v_bfe_u32 v44, v39, 16, 1
	v_add3_u32 v39, v39, v44, s76
	v_bfe_u32 v44, v38, 16, 1
	v_add3_u32 v38, v38, v44, s76
	v_lshrrev_b32_e32 v38, 16, v38
	v_and_or_b32 v44, v39, s77, v38
	v_bfe_u32 v39, v40, 16, 1
	v_bfe_u32 v38, v41, 16, 1
	v_add3_u32 v39, v40, v39, s76
	v_add3_u32 v38, v41, v38, s76
	v_lshrrev_b32_e32 v39, 16, v39
	v_and_or_b32 v45, v38, s77, v39
	s_nop 1
	v_mfma_f32_16x16x32_bf16 v[2:5], v[34:37], v[42:45], v[2:5]
	v_mfma_f32_16x16x32_bf16 v[6:9], v[34:37], v[82:85], v[6:9]
	v_mfma_f32_16x16x32_bf16 v[10:13], v[34:37], v[78:81], v[10:13]
	v_mfma_f32_16x16x32_bf16 v[14:17], v[34:37], v[72:75], v[14:17]
	v_mfma_f32_16x16x32_bf16 v[18:21], v[34:37], v[68:71], v[18:21]
	v_mfma_f32_16x16x32_bf16 v[22:25], v[34:37], v[64:67], v[22:25]
	v_mfma_f32_16x16x32_bf16 v[26:29], v[34:37], v[60:63], v[26:29]
	v_mfma_f32_16x16x32_bf16 v[30:33], v[34:37], v[46:49], v[30:33]
	v_lshl_or_b32 v54, s86, 20, v77
	v_cvt_pk_bf16_f32 v2, v2, v3
	v_cvt_pk_bf16_f32 v3, v4, v5
	v_lshl_add_u64 v[4:5], s[90:91], 0, v[54:55]
	s_lshl_b32 s6, s85, 1
	v_lshl_add_u64 v[4:5], v[4:5], 0, s[6:7]
	v_lshl_add_u64 v[4:5], v[4:5], 0, v[58:59]
	v_add_co_u32_e32 v34, vcc, s78, v4
	s_add_i32 s4, s4, s3
	s_nop 0
	v_addc_co_u32_e32 v35, vcc, 0, v5, vcc
	global_store_dwordx2 v[34:35], v[2:3], off
	v_cvt_pk_bf16_f32 v2, v6, v7
	v_add_co_u32_e32 v6, vcc, s79, v4
	v_cvt_pk_bf16_f32 v3, v8, v9
	s_add_i32 s5, s5, s35
	s_nop 0
	v_addc_co_u32_e32 v7, vcc, 0, v5, vcc
	global_store_dwordx2 v[6:7], v[2:3], off
	v_add_co_u32_e32 v6, vcc, s80, v4
	v_cvt_pk_bf16_f32 v2, v10, v11
	v_cvt_pk_bf16_f32 v3, v12, v13
	s_cmpk_lt_i32 s4, 0x1000
	s_nop 0
	v_addc_co_u32_e32 v7, vcc, 0, v5, vcc
	global_store_dwordx2 v[6:7], v[2:3], off
	v_add_co_u32_e32 v6, vcc, s81, v4
	v_cvt_pk_bf16_f32 v2, v14, v15
	v_cvt_pk_bf16_f32 v3, v16, v17
	s_nop 1
	v_addc_co_u32_e32 v7, vcc, 0, v5, vcc
	global_store_dwordx2 v[6:7], v[2:3], off
	v_add_co_u32_e32 v6, vcc, s82, v4
	v_cvt_pk_bf16_f32 v2, v18, v19
	v_cvt_pk_bf16_f32 v3, v20, v21
	s_nop 1
	v_addc_co_u32_e32 v7, vcc, 0, v5, vcc
	global_store_dwordx2 v[6:7], v[2:3], off
	v_add_co_u32_e32 v6, vcc, s83, v4
	v_cvt_pk_bf16_f32 v2, v22, v23
	v_cvt_pk_bf16_f32 v3, v24, v25
	s_nop 1
	v_addc_co_u32_e32 v7, vcc, 0, v5, vcc
	global_store_dwordx2 v[6:7], v[2:3], off
	v_add_co_u32_e32 v6, vcc, s84, v4
	v_cvt_pk_bf16_f32 v2, v26, v27
	v_cvt_pk_bf16_f32 v3, v28, v29
	s_nop 1
	v_addc_co_u32_e32 v7, vcc, 0, v5, vcc
	v_add_co_u32_e32 v4, vcc, 0xa5e0000, v4
	global_store_dwordx2 v[6:7], v[2:3], off
	s_nop 0
	v_addc_co_u32_e32 v5, vcc, 0, v5, vcc
	v_cvt_pk_bf16_f32 v2, v30, v31
	v_cvt_pk_bf16_f32 v3, v32, v33
	global_store_dwordx2 v[4:5], v[2:3], off
	s_cbranch_scc1 .LBB0_1498
	s_mov_b64 s[80:81], s[24:25]
	s_mov_b32 s82, s26
	s_mov_b32 s83, s27
	s_branch .LBB0_1500
.Lp13_conv:
	s_waitcnt vmcnt(0) lgkmcnt(0)
	v_and_b32_e32 v11, 63, v0
	v_lshrrev_b32_e32 v7, 6, v0
	v_lshlrev_b32_e32 v1, 4, v11
	v_readfirstlane_b32 s0, v7
	v_lshlrev_b32_e32 v2, 2, v11
	v_add_u32_e32 v3, 0x1000, v1
	v_add_u32_e32 v4, 0x2000, v1
	v_add_u32_e32 v5, 0x3000, v1
	v_mov_b32_e32 v10, 0
	v_cmp_eq_u32_e64 s[12:13], 0, v11
	s_lshl_b32 s1, s2, 2
	s_add_i32 s4, s1, s0
	s_addk_i32 s4, 0x7800
	s_mov_b32 s14, 0x43800000
	s_lshl_b32 s1, s4, 14
	s_add_u32 s6, s84, s1
	s_addc_u32 s7, s85, 0
	global_load_dwordx4 v[40:43], v1, s[6:7]
	global_load_dwordx4 v[44:47], v1, s[6:7] offset:1024
	global_load_dwordx4 v[48:51], v1, s[6:7] offset:2048
	global_load_dwordx4 v[52:55], v1, s[6:7] offset:3072
	global_load_dwordx4 v[56:59], v3, s[6:7]
	global_load_dwordx4 v[60:63], v3, s[6:7] offset:1024
	global_load_dwordx4 v[64:67], v3, s[6:7] offset:2048
	global_load_dwordx4 v[68:71], v3, s[6:7] offset:3072
	global_load_dwordx4 v[72:75], v4, s[6:7]
	global_load_dwordx4 v[76:79], v4, s[6:7] offset:1024
	global_load_dwordx4 v[80:83], v4, s[6:7] offset:2048
	global_load_dwordx4 v[84:87], v4, s[6:7] offset:3072
	global_load_dwordx4 v[88:91], v5, s[6:7]
	global_load_dwordx4 v[92:95], v5, s[6:7] offset:1024
	global_load_dwordx4 v[96:99], v5, s[6:7] offset:2048
	global_load_dwordx4 v[100:103], v5, s[6:7] offset:3072
	s_add_i32 s5, s4, 1024
	s_lshl_b32 s1, s5, 14
	s_add_u32 s6, s84, s1
	s_addc_u32 s7, s85, 0
	global_load_dwordx4 v[104:107], v1, s[6:7]
	global_load_dwordx4 v[108:111], v1, s[6:7] offset:1024
	global_load_dwordx4 v[112:115], v1, s[6:7] offset:2048
	global_load_dwordx4 v[116:119], v1, s[6:7] offset:3072
	global_load_dwordx4 v[120:123], v3, s[6:7]
	global_load_dwordx4 v[124:127], v3, s[6:7] offset:1024
	global_load_dwordx4 v[128:131], v3, s[6:7] offset:2048
	global_load_dwordx4 v[132:135], v3, s[6:7] offset:3072
	global_load_dwordx4 v[136:139], v4, s[6:7]
	global_load_dwordx4 v[140:143], v4, s[6:7] offset:1024
	global_load_dwordx4 v[144:147], v4, s[6:7] offset:2048
	global_load_dwordx4 v[148:151], v4, s[6:7] offset:3072
	global_load_dwordx4 v[152:155], v5, s[6:7]
	global_load_dwordx4 v[156:159], v5, s[6:7] offset:1024
	global_load_dwordx4 v[160:163], v5, s[6:7] offset:2048
	global_load_dwordx4 v[164:167], v5, s[6:7] offset:3072
	s_waitcnt vmcnt(31)
; template <int CTRL> __device__ __forceinline__ unsigned dppu(unsigned x) { return (unsigned)__builtin_amdgcn_mov_dpp((int)x, CTRL, 0xf, 0xf, true); }
; __device__ __forceinline__ unsigned max64u(unsigned x) {
;     x = umax_u(x, dppu<DPP_XOR1>(x)); x = umax_u(x, dppu<DPP_XOR2>(x)); x = umax_u(x, dppu<DPP_HMIRROR>(x)); x = umax_u(x, dppu<DPP_MIRROR>(x));
;     auto s = __builtin_amdgcn_permlane16_swap(x, x, false, false); x = umax_u(s[0], s[1]);
;     auto t = __builtin_amdgcn_permlane32_swap(x, x, false, false); return umax_u(t[0], t[1]);
; }
; __device__ __forceinline__ void peer_row_store(const f32x4 (&v)[16], unsigned char* ws, int it, int layer, int lane) {
;     const int tbl = it >= NEXP, r = it - tbl * NEXP + layer * NEXP;
;     float am = 0.f;
; #pragma unroll
;     for (int j = 0; j < 16; ++j) am = fmaxf(fmaxf(am, fmaxf(fabsf(v[j][0]), fabsf(v[j][1]))), fmaxf(fabsf(v[j][2]), fabsf(v[j][3])));
;     am = __uint_as_float(max64u(__float_as_uint(am)));
;     const float q = am > 0.f ? 256.0f / am : 0.f;
;     unsigned* dst = (unsigned*)(ws + (tbl ? WS_PV : WS_PU) + (size_t)r * D) + lane;
;     if (tbl) {
;         const int rl = it - NEXP;
;         unsigned char* pvl = ws + WS_PV + (size_t)layer * NEXP * D + (size_t)rl * 8 + (lane & 1) * 4;
;         unsigned char* pvg = ws + WS_PV + (size_t)layer * NEXP * D + (size_t)NEXP * 2048 + (size_t)rl * 2048 + 4 * lane;
; #pragma unroll
;         for (int j = 0; j < 16; ++j) { int w = __builtin_amdgcn_cvt_pk_bf8_f32(v[j][0] * q, v[j][1] * q, 0, false); w = __builtin_amdgcn_cvt_pk_bf8_f32(v[j][2] * q, v[j][3] * q, w, true);
;             if (j < 8) *(unsigned*)(pvl + (size_t)((lane >> 1) + 32 * j) * (NEXP * 8)) = (unsigned)w;
;             else *(unsigned*)(pvg + 256 * (j - 8)) = (unsigned)w; }
;     } else {
; #pragma unroll
;         for (int j = 0; j < 16; ++j) { int w = __builtin_amdgcn_cvt_pk_fp8_f32(v[j][0] * q, v[j][1] * q, 0, false); w = __builtin_amdgcn_cvt_pk_fp8_f32(v[j][2] * q, v[j][3] * q, w, true); dst[64 * j] = (unsigned)w; }
;     }
;     if (lane == 0) ((float*)(ws + (tbl ? WS_SV : WS_SU)))[r] = am * (1.0f / 256.0f);
; }
	v_max3_f32 v6, |v40|, |v41|, 0
	v_max3_f32 v6, |v42|, |v43|, v6
	s_waitcnt vmcnt(30)
	v_max3_f32 v6, |v44|, |v45|, v6
	v_max3_f32 v6, |v46|, |v47|, v6
	s_waitcnt vmcnt(29)
	v_max3_f32 v6, |v48|, |v49|, v6
	v_max3_f32 v6, |v50|, |v51|, v6
	s_waitcnt vmcnt(28)
	v_max3_f32 v6, |v52|, |v53|, v6
	v_max3_f32 v6, |v54|, |v55|, v6
	s_waitcnt vmcnt(27)
	v_max3_f32 v6, |v56|, |v57|, v6
	v_max3_f32 v6, |v58|, |v59|, v6
	s_waitcnt vmcnt(26)
	v_max3_f32 v6, |v60|, |v61|, v6
	v_max3_f32 v6, |v62|, |v63|, v6
	s_waitcnt vmcnt(25)
	v_max3_f32 v6, |v64|, |v65|, v6
	v_max3_f32 v6, |v66|, |v67|, v6
	s_waitcnt vmcnt(24)
	v_max3_f32 v6, |v68|, |v69|, v6
	v_max3_f32 v6, |v70|, |v71|, v6
	s_waitcnt vmcnt(23)
	v_max3_f32 v6, |v72|, |v73|, v6
	v_max3_f32 v6, |v74|, |v75|, v6
	s_waitcnt vmcnt(22)
	v_max3_f32 v6, |v76|, |v77|, v6
	v_max3_f32 v6, |v78|, |v79|, v6
	s_waitcnt vmcnt(21)
	v_max3_f32 v6, |v80|, |v81|, v6
	v_max3_f32 v6, |v82|, |v83|, v6
	s_waitcnt vmcnt(20)
	v_max3_f32 v6, |v84|, |v85|, v6
	v_max3_f32 v6, |v86|, |v87|, v6
	s_waitcnt vmcnt(19)
	v_max3_f32 v6, |v88|, |v89|, v6
	v_max3_f32 v6, |v90|, |v91|, v6
	s_waitcnt vmcnt(18)
	v_max3_f32 v6, |v92|, |v93|, v6
	v_max3_f32 v6, |v94|, |v95|, v6
	s_waitcnt vmcnt(17)
	v_max3_f32 v6, |v96|, |v97|, v6
	v_max3_f32 v6, |v98|, |v99|, v6
	s_waitcnt vmcnt(16)
	v_max3_f32 v6, |v100|, |v101|, v6
	v_max3_f32 v6, |v102|, |v103|, v6
	s_nop 1
	v_max_u32_dpp v6, v6, v6 quad_perm:[1,0,3,2] row_mask:0xf bank_mask:0xf bound_ctrl:1
	s_nop 1
	v_max_u32_dpp v6, v6, v6 quad_perm:[2,3,0,1] row_mask:0xf bank_mask:0xf bound_ctrl:1
	s_nop 1
	v_max_u32_dpp v6, v6, v6 row_half_mirror row_mask:0xf bank_mask:0xf bound_ctrl:1
	s_nop 1
	v_max_u32_dpp v6, v6, v6 row_mirror row_mask:0xf bank_mask:0xf bound_ctrl:1
	s_nop 1
	v_mov_b32_e32 v7, v6
	s_nop 1
	v_permlane16_swap_b32_e32 v6, v7
	v_max_u32_e32 v6, v6, v7
	v_mov_b32_e32 v7, v6
	s_nop 1
	v_permlane32_swap_b32_e32 v6, v7
	v_max_u32_e32 v6, v6, v7
	v_div_scale_f32 v12, s[16:17], v6, v6, s14
	v_rcp_f32_e32 v13, v12
	s_nop 0
	v_fma_f32 v14, -v12, v13, 1.0
	v_fmac_f32_e32 v13, v14, v13
	v_div_scale_f32 v14, vcc, s14, v6, s14
	v_mul_f32_e32 v15, v14, v13
	v_fma_f32 v16, -v12, v15, v14
	v_fmac_f32_e32 v15, v16, v13
	v_fma_f32 v12, -v12, v15, v14
	v_div_fmas_f32 v12, v12, v13, v15
	v_div_fixup_f32 v9, v12, v6, s14
	v_cmp_lt_f32_e32 vcc, 0, v6
	s_nop 1
	v_cndmask_b32_e32 v9, 0, v9, vcc
	s_lshl_b32 s1, s4, 12
	s_add_u32 s8, s90, 0xba00000
	s_addc_u32 s9, s91, 0
	s_add_u32 s8, s8, s1
	s_addc_u32 s9, s9, 0
	s_lshl_b32 s1, s4, 2
	s_add_u32 s10, s90, 0x1ba00000
	s_addc_u32 s11, s91, 0
	s_add_u32 s10, s10, s1
	s_addc_u32 s11, s11, 0
	v_mul_f32_e32 v40, v40, v9
	v_mul_f32_e32 v41, v41, v9
	v_mul_f32_e32 v42, v42, v9
	v_mul_f32_e32 v43, v43, v9
	v_mov_b32_e32 v20, v10
	v_cvt_pk_fp8_f32 v20, v40, v41
	v_mul_f32_e32 v44, v44, v9
	v_mul_f32_e32 v45, v45, v9
	v_mul_f32_e32 v46, v46, v9
	v_mul_f32_e32 v47, v47, v9
	v_mov_b32_e32 v21, v10
	v_cvt_pk_fp8_f32 v21, v44, v45
	v_cvt_pk_fp8_f32 v20, v42, v43 op_sel:[0,0,1]
	v_mul_f32_e32 v48, v48, v9
	v_mul_f32_e32 v49, v49, v9
	v_mul_f32_e32 v50, v50, v9
	v_mul_f32_e32 v51, v51, v9
	v_mov_b32_e32 v22, v10
	v_cvt_pk_fp8_f32 v22, v48, v49
	v_cvt_pk_fp8_f32 v21, v46, v47 op_sel:[0,0,1]
	v_mul_f32_e32 v52, v52, v9
	v_mul_f32_e32 v53, v53, v9
	v_mul_f32_e32 v54, v54, v9
	v_mul_f32_e32 v55, v55, v9
	v_mov_b32_e32 v23, v10
	v_cvt_pk_fp8_f32 v23, v52, v53
	v_cvt_pk_fp8_f32 v22, v50, v51 op_sel:[0,0,1]
	v_mul_f32_e32 v56, v56, v9
	v_mul_f32_e32 v57, v57, v9
	v_mul_f32_e32 v58, v58, v9
	v_mul_f32_e32 v59, v59, v9
	v_mov_b32_e32 v24, v10
	v_cvt_pk_fp8_f32 v24, v56, v57
	v_cvt_pk_fp8_f32 v23, v54, v55 op_sel:[0,0,1]
	v_mul_f32_e32 v60, v60, v9
	v_mul_f32_e32 v61, v61, v9
	v_mul_f32_e32 v62, v62, v9
	v_mul_f32_e32 v63, v63, v9
	v_mov_b32_e32 v25, v10
	v_cvt_pk_fp8_f32 v25, v60, v61
	v_cvt_pk_fp8_f32 v24, v58, v59 op_sel:[0,0,1]
	v_mul_f32_e32 v64, v64, v9
	v_mul_f32_e32 v65, v65, v9
	v_mul_f32_e32 v66, v66, v9
	v_mul_f32_e32 v67, v67, v9
	v_mov_b32_e32 v26, v10
	v_cvt_pk_fp8_f32 v26, v64, v65
	v_cvt_pk_fp8_f32 v25, v62, v63 op_sel:[0,0,1]
	v_mul_f32_e32 v68, v68, v9
	v_mul_f32_e32 v69, v69, v9
	v_mul_f32_e32 v70, v70, v9
	v_mul_f32_e32 v71, v71, v9
	v_mov_b32_e32 v27, v10
	v_cvt_pk_fp8_f32 v27, v68, v69
	v_cvt_pk_fp8_f32 v26, v66, v67 op_sel:[0,0,1]
	v_mul_f32_e32 v72, v72, v9
	v_mul_f32_e32 v73, v73, v9
	v_mul_f32_e32 v74, v74, v9
	v_mul_f32_e32 v75, v75, v9
	v_mov_b32_e32 v28, v10
	v_cvt_pk_fp8_f32 v28, v72, v73
	v_cvt_pk_fp8_f32 v27, v70, v71 op_sel:[0,0,1]
	v_mul_f32_e32 v76, v76, v9
	v_mul_f32_e32 v77, v77, v9
	v_mul_f32_e32 v78, v78, v9
	v_mul_f32_e32 v79, v79, v9
	v_mov_b32_e32 v29, v10
	v_cvt_pk_fp8_f32 v29, v76, v77
	v_cvt_pk_fp8_f32 v28, v74, v75 op_sel:[0,0,1]
	v_mul_f32_e32 v80, v80, v9
	v_mul_f32_e32 v81, v81, v9
	v_mul_f32_e32 v82, v82, v9
	v_mul_f32_e32 v83, v83, v9
	v_mov_b32_e32 v30, v10
	v_cvt_pk_fp8_f32 v30, v80, v81
	v_cvt_pk_fp8_f32 v29, v78, v79 op_sel:[0,0,1]
	v_mul_f32_e32 v84, v84, v9
	v_mul_f32_e32 v85, v85, v9
	v_mul_f32_e32 v86, v86, v9
	v_mul_f32_e32 v87, v87, v9
	v_mov_b32_e32 v31, v10
	v_cvt_pk_fp8_f32 v31, v84, v85
	v_cvt_pk_fp8_f32 v30, v82, v83 op_sel:[0,0,1]
	v_mul_f32_e32 v88, v88, v9
	v_mul_f32_e32 v89, v89, v9
	v_mul_f32_e32 v90, v90, v9
	v_mul_f32_e32 v91, v91, v9
	v_mov_b32_e32 v32, v10
	v_cvt_pk_fp8_f32 v32, v88, v89
	v_cvt_pk_fp8_f32 v31, v86, v87 op_sel:[0,0,1]
	v_mul_f32_e32 v92, v92, v9
	v_mul_f32_e32 v93, v93, v9
	v_mul_f32_e32 v94, v94, v9
	v_mul_f32_e32 v95, v95, v9
	v_mov_b32_e32 v33, v10
	v_cvt_pk_fp8_f32 v33, v92, v93
	v_cvt_pk_fp8_f32 v32, v90, v91 op_sel:[0,0,1]
	v_mul_f32_e32 v96, v96, v9
	v_mul_f32_e32 v97, v97, v9
	v_mul_f32_e32 v98, v98, v9
	v_mul_f32_e32 v99, v99, v9
	v_mov_b32_e32 v34, v10
	v_cvt_pk_fp8_f32 v34, v96, v97
	v_cvt_pk_fp8_f32 v33, v94, v95 op_sel:[0,0,1]
	v_mul_f32_e32 v100, v100, v9
	v_mul_f32_e32 v101, v101, v9
	v_mul_f32_e32 v102, v102, v9
	v_mul_f32_e32 v103, v103, v9
	v_mov_b32_e32 v35, v10
	v_cvt_pk_fp8_f32 v35, v100, v101
	v_cvt_pk_fp8_f32 v34, v98, v99 op_sel:[0,0,1]
	v_cvt_pk_fp8_f32 v35, v102, v103 op_sel:[0,0,1]
	s_nop 0
	v_mul_f32_e32 v8, 0x3b800000, v6
	global_store_dword v2, v20, s[8:9]
	global_store_dword v2, v21, s[8:9] offset:256
	global_store_dword v2, v22, s[8:9] offset:512
	global_store_dword v2, v23, s[8:9] offset:768
	global_store_dword v2, v24, s[8:9] offset:1024
	global_store_dword v2, v25, s[8:9] offset:1280
	global_store_dword v2, v26, s[8:9] offset:1536
	global_store_dword v2, v27, s[8:9] offset:1792
	global_store_dword v2, v28, s[8:9] offset:2048
	global_store_dword v2, v29, s[8:9] offset:2304
	global_store_dword v2, v30, s[8:9] offset:2560
	global_store_dword v2, v31, s[8:9] offset:2816
	global_store_dword v2, v32, s[8:9] offset:3072
	global_store_dword v2, v33, s[8:9] offset:3328
	global_store_dword v2, v34, s[8:9] offset:3584
	global_store_dword v2, v35, s[8:9] offset:3840
	s_mov_b64 s[18:19], exec
	s_mov_b64 exec, s[12:13]
	global_store_dword v10, v8, s[10:11]
	s_mov_b64 exec, s[18:19]
	s_mov_b32 s4, s5
	s_waitcnt vmcnt(32)
; __device__ __forceinline__ void peer_row_store(const f32x4 (&v)[16], unsigned char* ws, int it, int layer, int lane) {
;     const int tbl = it >= NEXP, r = it - tbl * NEXP + layer * NEXP;
;     float am = 0.f;
; #pragma unroll
;     for (int j = 0; j < 16; ++j) am = fmaxf(fmaxf(am, fmaxf(fabsf(v[j][0]), fabsf(v[j][1]))), fmaxf(fabsf(v[j][2]), fabsf(v[j][3])));
;     am = __uint_as_float(max64u(__float_as_uint(am)));
;     const float q = am > 0.f ? 256.0f / am : 0.f;
	v_max3_f32 v6, |v104|, |v105|, 0
	v_max3_f32 v6, |v106|, |v107|, v6
	s_waitcnt vmcnt(31)
	v_max3_f32 v6, |v108|, |v109|, v6
	v_max3_f32 v6, |v110|, |v111|, v6
	s_waitcnt vmcnt(30)
	v_max3_f32 v6, |v112|, |v113|, v6
	v_max3_f32 v6, |v114|, |v115|, v6
	s_waitcnt vmcnt(29)
	v_max3_f32 v6, |v116|, |v117|, v6
	v_max3_f32 v6, |v118|, |v119|, v6
	s_waitcnt vmcnt(28)
	v_max3_f32 v6, |v120|, |v121|, v6
	v_max3_f32 v6, |v122|, |v123|, v6
	s_waitcnt vmcnt(27)
	v_max3_f32 v6, |v124|, |v125|, v6
	v_max3_f32 v6, |v126|, |v127|, v6
	s_waitcnt vmcnt(26)
	v_max3_f32 v6, |v128|, |v129|, v6
	v_max3_f32 v6, |v130|, |v131|, v6
	s_waitcnt vmcnt(25)
	v_max3_f32 v6, |v132|, |v133|, v6
	v_max3_f32 v6, |v134|, |v135|, v6
	s_waitcnt vmcnt(24)
	v_max3_f32 v6, |v136|, |v137|, v6
	v_max3_f32 v6, |v138|, |v139|, v6
	s_waitcnt vmcnt(23)
	v_max3_f32 v6, |v140|, |v141|, v6
	v_max3_f32 v6, |v142|, |v143|, v6
	s_waitcnt vmcnt(22)
	v_max3_f32 v6, |v144|, |v145|, v6
	v_max3_f32 v6, |v146|, |v147|, v6
	s_waitcnt vmcnt(21)
	v_max3_f32 v6, |v148|, |v149|, v6
	v_max3_f32 v6, |v150|, |v151|, v6
	s_waitcnt vmcnt(20)
	v_max3_f32 v6, |v152|, |v153|, v6
	v_max3_f32 v6, |v154|, |v155|, v6
	s_waitcnt vmcnt(19)
	v_max3_f32 v6, |v156|, |v157|, v6
	v_max3_f32 v6, |v158|, |v159|, v6
	s_waitcnt vmcnt(18)
	v_max3_f32 v6, |v160|, |v161|, v6
	v_max3_f32 v6, |v162|, |v163|, v6
	s_waitcnt vmcnt(17)
; template <int CTRL> __device__ __forceinline__ unsigned dppu(unsigned x) { return (unsigned)__builtin_amdgcn_mov_dpp((int)x, CTRL, 0xf, 0xf, true); }
; __device__ __forceinline__ unsigned max64u(unsigned x) {
;     x = umax_u(x, dppu<DPP_XOR1>(x)); x = umax_u(x, dppu<DPP_XOR2>(x)); x = umax_u(x, dppu<DPP_HMIRROR>(x)); x = umax_u(x, dppu<DPP_MIRROR>(x));
;     auto s = __builtin_amdgcn_permlane16_swap(x, x, false, false); x = umax_u(s[0], s[1]);
;     auto t = __builtin_amdgcn_permlane32_swap(x, x, false, false); return umax_u(t[0], t[1]);
; }
; __device__ __forceinline__ void peer_row_store(const f32x4 (&v)[16], unsigned char* ws, int it, int layer, int lane) {
;     const int tbl = it >= NEXP, r = it - tbl * NEXP + layer * NEXP;
;     float am = 0.f;
; #pragma unroll
;     for (int j = 0; j < 16; ++j) am = fmaxf(fmaxf(am, fmaxf(fabsf(v[j][0]), fabsf(v[j][1]))), fmaxf(fabsf(v[j][2]), fabsf(v[j][3])));
;     am = __uint_as_float(max64u(__float_as_uint(am)));
;     const float q = am > 0.f ? 256.0f / am : 0.f;
;     unsigned* dst = (unsigned*)(ws + (tbl ? WS_PV : WS_PU) + (size_t)r * D) + lane;
;     if (tbl) {
;         const int rl = it - NEXP;
;         unsigned char* pvl = ws + WS_PV + (size_t)layer * NEXP * D + (size_t)rl * 8 + (lane & 1) * 4;
;         unsigned char* pvg = ws + WS_PV + (size_t)layer * NEXP * D + (size_t)NEXP * 2048 + (size_t)rl * 2048 + 4 * lane;
; #pragma unroll
;         for (int j = 0; j < 16; ++j) { int w = __builtin_amdgcn_cvt_pk_bf8_f32(v[j][0] * q, v[j][1] * q, 0, false); w = __builtin_amdgcn_cvt_pk_bf8_f32(v[j][2] * q, v[j][3] * q, w, true);
;             if (j < 8) *(unsigned*)(pvl + (size_t)((lane >> 1) + 32 * j) * (NEXP * 8)) = (unsigned)w;
;             else *(unsigned*)(pvg + 256 * (j - 8)) = (unsigned)w; }
;     } else {
; #pragma unroll
;         for (int j = 0; j < 16; ++j) { int w = __builtin_amdgcn_cvt_pk_fp8_f32(v[j][0] * q, v[j][1] * q, 0, false); w = __builtin_amdgcn_cvt_pk_fp8_f32(v[j][2] * q, v[j][3] * q, w, true); dst[64 * j] = (unsigned)w; }
;     }
;     if (lane == 0) ((float*)(ws + (tbl ? WS_SV : WS_SU)))[r] = am * (1.0f / 256.0f);
; }
	v_max3_f32 v6, |v164|, |v165|, v6
	v_max3_f32 v6, |v166|, |v167|, v6
	s_nop 1
	v_max_u32_dpp v6, v6, v6 quad_perm:[1,0,3,2] row_mask:0xf bank_mask:0xf bound_ctrl:1
	s_nop 1
	v_max_u32_dpp v6, v6, v6 quad_perm:[2,3,0,1] row_mask:0xf bank_mask:0xf bound_ctrl:1
	s_nop 1
	v_max_u32_dpp v6, v6, v6 row_half_mirror row_mask:0xf bank_mask:0xf bound_ctrl:1
	s_nop 1
	v_max_u32_dpp v6, v6, v6 row_mirror row_mask:0xf bank_mask:0xf bound_ctrl:1
	s_nop 1
	v_mov_b32_e32 v7, v6
	s_nop 1
	v_permlane16_swap_b32_e32 v6, v7
	v_max_u32_e32 v6, v6, v7
	v_mov_b32_e32 v7, v6
	s_nop 1
	v_permlane32_swap_b32_e32 v6, v7
	v_max_u32_e32 v6, v6, v7
	v_div_scale_f32 v12, s[16:17], v6, v6, s14
	v_rcp_f32_e32 v13, v12
	s_nop 0
	v_fma_f32 v14, -v12, v13, 1.0
	v_fmac_f32_e32 v13, v14, v13
	v_div_scale_f32 v14, vcc, s14, v6, s14
	v_mul_f32_e32 v15, v14, v13
	v_fma_f32 v16, -v12, v15, v14
	v_fmac_f32_e32 v15, v16, v13
	v_fma_f32 v12, -v12, v15, v14
	v_div_fmas_f32 v12, v12, v13, v15
	v_div_fixup_f32 v9, v12, v6, s14
	v_cmp_lt_f32_e32 vcc, 0, v6
	s_nop 1
	v_cndmask_b32_e32 v9, 0, v9, vcc
	s_lshl_b32 s1, s4, 12
	s_add_u32 s8, s90, 0xba00000
	s_addc_u32 s9, s91, 0
	s_add_u32 s8, s8, s1
	s_addc_u32 s9, s9, 0
	s_lshl_b32 s1, s4, 2
	s_add_u32 s10, s90, 0x1ba00000
	s_addc_u32 s11, s91, 0
	s_add_u32 s10, s10, s1
	s_addc_u32 s11, s11, 0
	v_mul_f32_e32 v104, v104, v9
	v_mul_f32_e32 v105, v105, v9
	v_mul_f32_e32 v106, v106, v9
	v_mul_f32_e32 v107, v107, v9
	v_mov_b32_e32 v20, v10
	v_cvt_pk_fp8_f32 v20, v104, v105
	v_mul_f32_e32 v108, v108, v9
	v_mul_f32_e32 v109, v109, v9
	v_mul_f32_e32 v110, v110, v9
	v_mul_f32_e32 v111, v111, v9
	v_mov_b32_e32 v21, v10
	v_cvt_pk_fp8_f32 v21, v108, v109
	v_cvt_pk_fp8_f32 v20, v106, v107 op_sel:[0,0,1]
	v_mul_f32_e32 v112, v112, v9
	v_mul_f32_e32 v113, v113, v9
	v_mul_f32_e32 v114, v114, v9
	v_mul_f32_e32 v115, v115, v9
	v_mov_b32_e32 v22, v10
	v_cvt_pk_fp8_f32 v22, v112, v113
	v_cvt_pk_fp8_f32 v21, v110, v111 op_sel:[0,0,1]
	v_mul_f32_e32 v116, v116, v9
	v_mul_f32_e32 v117, v117, v9
	v_mul_f32_e32 v118, v118, v9
	v_mul_f32_e32 v119, v119, v9
	v_mov_b32_e32 v23, v10
	v_cvt_pk_fp8_f32 v23, v116, v117
	v_cvt_pk_fp8_f32 v22, v114, v115 op_sel:[0,0,1]
	v_mul_f32_e32 v120, v120, v9
	v_mul_f32_e32 v121, v121, v9
	v_mul_f32_e32 v122, v122, v9
	v_mul_f32_e32 v123, v123, v9
	v_mov_b32_e32 v24, v10
	v_cvt_pk_fp8_f32 v24, v120, v121
	v_cvt_pk_fp8_f32 v23, v118, v119 op_sel:[0,0,1]
	v_mul_f32_e32 v124, v124, v9
	v_mul_f32_e32 v125, v125, v9
	v_mul_f32_e32 v126, v126, v9
	v_mul_f32_e32 v127, v127, v9
	v_mov_b32_e32 v25, v10
	v_cvt_pk_fp8_f32 v25, v124, v125
	v_cvt_pk_fp8_f32 v24, v122, v123 op_sel:[0,0,1]
	v_mul_f32_e32 v128, v128, v9
	v_mul_f32_e32 v129, v129, v9
	v_mul_f32_e32 v130, v130, v9
	v_mul_f32_e32 v131, v131, v9
	v_mov_b32_e32 v26, v10
	v_cvt_pk_fp8_f32 v26, v128, v129
	v_cvt_pk_fp8_f32 v25, v126, v127 op_sel:[0,0,1]
	v_mul_f32_e32 v132, v132, v9
	v_mul_f32_e32 v133, v133, v9
	v_mul_f32_e32 v134, v134, v9
	v_mul_f32_e32 v135, v135, v9
	v_mov_b32_e32 v27, v10
	v_cvt_pk_fp8_f32 v27, v132, v133
	v_cvt_pk_fp8_f32 v26, v130, v131 op_sel:[0,0,1]
	v_mul_f32_e32 v136, v136, v9
	v_mul_f32_e32 v137, v137, v9
	v_mul_f32_e32 v138, v138, v9
	v_mul_f32_e32 v139, v139, v9
	v_mov_b32_e32 v28, v10
	v_cvt_pk_fp8_f32 v28, v136, v137
	v_cvt_pk_fp8_f32 v27, v134, v135 op_sel:[0,0,1]
	v_mul_f32_e32 v140, v140, v9
	v_mul_f32_e32 v141, v141, v9
	v_mul_f32_e32 v142, v142, v9
	v_mul_f32_e32 v143, v143, v9
	v_mov_b32_e32 v29, v10
	v_cvt_pk_fp8_f32 v29, v140, v141
	v_cvt_pk_fp8_f32 v28, v138, v139 op_sel:[0,0,1]
	v_mul_f32_e32 v144, v144, v9
	v_mul_f32_e32 v145, v145, v9
	v_mul_f32_e32 v146, v146, v9
	v_mul_f32_e32 v147, v147, v9
	v_mov_b32_e32 v30, v10
	v_cvt_pk_fp8_f32 v30, v144, v145
	v_cvt_pk_fp8_f32 v29, v142, v143 op_sel:[0,0,1]
	v_mul_f32_e32 v148, v148, v9
	v_mul_f32_e32 v149, v149, v9
	v_mul_f32_e32 v150, v150, v9
	v_mul_f32_e32 v151, v151, v9
	v_mov_b32_e32 v31, v10
	v_cvt_pk_fp8_f32 v31, v148, v149
	v_cvt_pk_fp8_f32 v30, v146, v147 op_sel:[0,0,1]
	v_mul_f32_e32 v152, v152, v9
	v_mul_f32_e32 v153, v153, v9
	v_mul_f32_e32 v154, v154, v9
	v_mul_f32_e32 v155, v155, v9
	v_mov_b32_e32 v32, v10
	v_cvt_pk_fp8_f32 v32, v152, v153
	v_cvt_pk_fp8_f32 v31, v150, v151 op_sel:[0,0,1]
	v_mul_f32_e32 v156, v156, v9
	v_mul_f32_e32 v157, v157, v9
	v_mul_f32_e32 v158, v158, v9
	v_mul_f32_e32 v159, v159, v9
	v_mov_b32_e32 v33, v10
	v_cvt_pk_fp8_f32 v33, v156, v157
	v_cvt_pk_fp8_f32 v32, v154, v155 op_sel:[0,0,1]
	v_mul_f32_e32 v160, v160, v9
	v_mul_f32_e32 v161, v161, v9
	v_mul_f32_e32 v162, v162, v9
	v_mul_f32_e32 v163, v163, v9
	v_mov_b32_e32 v34, v10
	v_cvt_pk_fp8_f32 v34, v160, v161
	v_cvt_pk_fp8_f32 v33, v158, v159 op_sel:[0,0,1]
	v_mul_f32_e32 v164, v164, v9
	v_mul_f32_e32 v165, v165, v9
	v_mul_f32_e32 v166, v166, v9
	v_mul_f32_e32 v167, v167, v9
	v_mov_b32_e32 v35, v10
	v_cvt_pk_fp8_f32 v35, v164, v165
	v_cvt_pk_fp8_f32 v34, v162, v163 op_sel:[0,0,1]
	v_cvt_pk_fp8_f32 v35, v166, v167 op_sel:[0,0,1]
	s_nop 0
	v_mul_f32_e32 v8, 0x3b800000, v6
	global_store_dword v2, v20, s[8:9]
	global_store_dword v2, v21, s[8:9] offset:256
	global_store_dword v2, v22, s[8:9] offset:512
	global_store_dword v2, v23, s[8:9] offset:768
	global_store_dword v2, v24, s[8:9] offset:1024
	global_store_dword v2, v25, s[8:9] offset:1280
	global_store_dword v2, v26, s[8:9] offset:1536
	global_store_dword v2, v27, s[8:9] offset:1792
	global_store_dword v2, v28, s[8:9] offset:2048
	global_store_dword v2, v29, s[8:9] offset:2304
	global_store_dword v2, v30, s[8:9] offset:2560
	global_store_dword v2, v31, s[8:9] offset:2816
	global_store_dword v2, v32, s[8:9] offset:3072
	global_store_dword v2, v33, s[8:9] offset:3328
	global_store_dword v2, v34, s[8:9] offset:3584
	global_store_dword v2, v35, s[8:9] offset:3840
	s_mov_b64 s[18:19], exec
	s_mov_b64 exec, s[12:13]
	global_store_dword v10, v8, s[10:11]
	s_mov_b64 exec, s[18:19]
	s_waitcnt vmcnt(0)
